# speedup vs baseline: 1.0435x; 1.0060x over previous
.Lk_15:
	global_load_dword v66, v[62:63], off offset:4
	global_load_dword v67, v[62:63], off offset:260
	global_load_dword v68, v[62:63], off offset:516
	global_load_dword v69, v[62:63], off offset:772
	global_load_dword v70, v[64:65], off offset:4
	global_load_dword v71, v[64:65], off offset:260
	global_load_dword v72, v[64:65], off offset:516
	global_load_dword v73, v[64:65], off offset:772
	v_and_b32_e32 v62, 15, v0
	s_mov_b32 s8, 0x4038aa3b
	s_waitcnt vmcnt(11)
	v_pk_mul_f32 v[38:39], v[50:51], v[38:39]
	v_lshlrev_b32_e32 v57, 2, v1
	s_lshl_b32 s10, s34, 8
	v_lshlrev_b32_e32 v1, 4, v62
	v_pk_add_f32 v[52:53], v[52:53], v[54:55]
	v_pk_add_f32 v[54:55], v[58:59], v[60:61]
	s_mov_b32 s9, 0xbfb8aa3b
	s_waitcnt vmcnt(10)
	v_pk_mul_f32 v[46:47], v[50:51], v[46:47]
	v_pk_mul_f32 v[48:49], v[50:51], v[48:49]
	v_pk_mul_f32 v[40:41], v[50:51], v[40:41]
	s_waitcnt vmcnt(8)
	v_pk_mul_f32 v[42:43], v[50:51], v[42:43]
	v_pk_mul_f32 v[44:45], v[50:51], v[44:45]
	v_pk_mul_f32 v[34:35], v[50:51], v[34:35]
	v_pk_mul_f32 v[36:37], v[50:51], v[36:37]
	v_pk_mul_f32 v[30:31], v[50:51], v[30:31]
	v_pk_mul_f32 v[32:33], v[50:51], v[32:33]
	v_pk_mul_f32 v[18:19], v[50:51], v[18:19]
	v_pk_mul_f32 v[58:59], v[50:51], v[20:21]
	v_pk_mul_f32 v[60:61], v[50:51], v[26:27]
	v_pk_mul_f32 v[64:65], v[50:51], v[28:29]
	v_pk_mul_f32 v[74:75], v[50:51], v[22:23]
	v_pk_mul_f32 v[50:51], v[50:51], v[24:25]
	v_cvt_pk_f16_f32 v24, v38, v39
	v_or3_b32 v38, v1, v57, s10
	v_lshlrev_b32_e32 v82, 4, v80
	s_and_b64 vcc, exec, s[6:7]
	s_mov_b32 s6, s9
	v_cvt_pk_f16_f32 v25, v40, v41
	v_add_u32_e32 v81, 0x23280, v38
	s_mov_b64 s[4:5], -1
	v_pk_mul_f32 v[20:21], v[54:55], s[8:9]
	v_cvt_pk_f16_f32 v22, v46, v47
	v_cvt_pk_f16_f32 v23, v48, v49
	v_cvt_pk_f16_f32 v26, v42, v43
	v_cvt_pk_f16_f32 v27, v44, v45
	v_cvt_pk_f16_f32 v28, v34, v35
	v_cvt_pk_f16_f32 v29, v36, v37
	v_cvt_pk_f16_f32 v30, v30, v31
	v_cvt_pk_f16_f32 v31, v32, v33
	v_cvt_pk_f16_f32 v32, v18, v19
	v_cvt_pk_f16_f32 v33, v58, v59
	v_cvt_pk_f16_f32 v34, v60, v61
	v_cvt_pk_f16_f32 v35, v64, v65
	v_cvt_pk_f16_f32 v36, v74, v75
	v_cvt_pk_f16_f32 v37, v50, v51
	v_add_u32_e32 v75, 0x23280, v82
	v_pk_mul_f32 v[18:19], v[52:53], s[6:7] op_sel_hi:[1,0]
	s_waitcnt lgkmcnt(0)
	s_barrier
	s_waitcnt vmcnt(2)
	v_pk_add_f32 v[38:39], v[66:67], v[70:71]
	s_nop 0
	v_pk_mul_f32 v[38:39], v[38:39], s[6:7] op_sel_hi:[1,0]
	s_waitcnt vmcnt(0)
	v_pk_add_f32 v[40:41], v[68:69], v[72:73]
	s_nop 0
	v_pk_mul_f32 v[40:41], v[40:41], s[8:9]
	s_cbranch_vccz .Lk_134
	s_setprio 0
	v_lshrrev_b32_e32 v42, 4, v80
	v_lshlrev_b32_e32 v42, 5, v42
	global_load_dwordx4 v[44:47], v42, s[18:19]
	global_load_dwordx4 v[48:51], v42, s[18:19] offset:16
	global_load_dwordx4 v[52:55], v42, s[18:19] offset:128
	global_load_dwordx4 v[56:59], v42, s[18:19] offset:144
	s_load_dword s28, s[20:21], 0x0
	v_and_b32_e32 v43, 15, v80
	v_cmp_eq_u32_e32 vcc, 1, v43
	v_cmp_eq_u32_e64 s[4:5], 0, v43
	v_cmp_gt_u32_e64 s[30:31], 16, v80
	v_lshl_or_b32 v124, s3, 4, v43
	v_mul_u32_u24_e32 v124, 0x708, v124
	v_lshlrev_b32_e32 v74, 2, v43
	v_add_u32_e32 v74, 0x1c200, v74
	v_mov_b32_e32 v72, 0x3fe10966
	v_mov_b32_e32 v73, 0xbfe10966
	v_mov_b32_e32 v92, 0xc038aa3b
	v_mov_b32_e32 v93, 0xc038aa3b
	s_mov_b32 s8, 0x4038aa3b
	s_mov_b32 s9, 0
	v_mov_b32_e32 v64, 0
	v_mov_b32_e32 v65, 0
	s_mov_b32 s12, 4
	s_waitcnt vmcnt(0) lgkmcnt(0)
	v_cvt_f16_f32_e32 v60, v44
	v_cvt_f32_f16_e32 v61, v60
	v_sub_f32_e32 v61, v44, v61
	v_cvt_f16_f32_e32 v61, v61
	v_cndmask_b32_e32 v61, 0, v61, vcc
	v_cndmask_b32_e64 v94, v61, v60, s[4:5]
	v_cvt_f16_f32_e32 v60, v45
	v_cvt_f32_f16_e32 v61, v60
	v_sub_f32_e32 v61, v45, v61
	v_cvt_f16_f32_e32 v61, v61
	v_cndmask_b32_e32 v61, 0, v61, vcc
	v_cndmask_b32_e64 v95, v61, v60, s[4:5]
	v_cvt_f16_f32_e32 v60, v46
	v_cvt_f32_f16_e32 v61, v60
	v_sub_f32_e32 v61, v46, v61
	v_cvt_f16_f32_e32 v61, v61
	v_cndmask_b32_e32 v61, 0, v61, vcc
	v_cndmask_b32_e64 v96, v61, v60, s[4:5]
	v_cvt_f16_f32_e32 v60, v47
	v_cvt_f32_f16_e32 v61, v60
	v_sub_f32_e32 v61, v47, v61
	v_cvt_f16_f32_e32 v61, v61
	v_cndmask_b32_e32 v61, 0, v61, vcc
	v_cndmask_b32_e64 v97, v61, v60, s[4:5]
	v_cvt_f16_f32_e32 v60, v48
	v_cvt_f32_f16_e32 v61, v60
	v_sub_f32_e32 v61, v48, v61
	v_cvt_f16_f32_e32 v61, v61
	v_cndmask_b32_e32 v61, 0, v61, vcc
	v_cndmask_b32_e64 v98, v61, v60, s[4:5]
	v_cvt_f16_f32_e32 v60, v49
	v_cvt_f32_f16_e32 v61, v60
	v_sub_f32_e32 v61, v49, v61
	v_cvt_f16_f32_e32 v61, v61
	v_cndmask_b32_e32 v61, 0, v61, vcc
	v_cndmask_b32_e64 v99, v61, v60, s[4:5]
	v_cvt_f16_f32_e32 v60, v50
	v_cvt_f32_f16_e32 v61, v60
	v_sub_f32_e32 v61, v50, v61
	v_cvt_f16_f32_e32 v61, v61
	v_cndmask_b32_e32 v61, 0, v61, vcc
	v_cndmask_b32_e64 v100, v61, v60, s[4:5]
	v_cvt_f16_f32_e32 v60, v51
	v_cvt_f32_f16_e32 v61, v60
	v_sub_f32_e32 v61, v51, v61
	v_cvt_f16_f32_e32 v61, v61
	v_cndmask_b32_e32 v61, 0, v61, vcc
	v_cndmask_b32_e64 v101, v61, v60, s[4:5]
	v_cvt_f16_f32_e32 v60, v52
	v_cvt_f32_f16_e32 v61, v60
	v_sub_f32_e32 v61, v52, v61
	v_cvt_f16_f32_e32 v61, v61
	v_cndmask_b32_e32 v61, 0, v61, vcc
	v_cndmask_b32_e64 v102, v61, v60, s[4:5]
	v_cvt_f16_f32_e32 v60, v53
	v_cvt_f32_f16_e32 v61, v60
	v_sub_f32_e32 v61, v53, v61
	v_cvt_f16_f32_e32 v61, v61
	v_cndmask_b32_e32 v61, 0, v61, vcc
	v_cndmask_b32_e64 v103, v61, v60, s[4:5]
	v_cvt_f16_f32_e32 v60, v54
	v_cvt_f32_f16_e32 v61, v60
	v_sub_f32_e32 v61, v54, v61
	v_cvt_f16_f32_e32 v61, v61
	v_cndmask_b32_e32 v61, 0, v61, vcc
	v_cndmask_b32_e64 v104, v61, v60, s[4:5]
	v_cvt_f16_f32_e32 v60, v55
	v_cvt_f32_f16_e32 v61, v60
	v_sub_f32_e32 v61, v55, v61
	v_cvt_f16_f32_e32 v61, v61
	v_cndmask_b32_e32 v61, 0, v61, vcc
	v_cndmask_b32_e64 v105, v61, v60, s[4:5]
	v_cvt_f16_f32_e32 v60, v56
	v_cvt_f32_f16_e32 v61, v60
	v_sub_f32_e32 v61, v56, v61
	v_cvt_f16_f32_e32 v61, v61
	v_cndmask_b32_e32 v61, 0, v61, vcc
	v_cndmask_b32_e64 v106, v61, v60, s[4:5]
	v_cvt_f16_f32_e32 v60, v57
	v_cvt_f32_f16_e32 v61, v60
	v_sub_f32_e32 v61, v57, v61
	v_cvt_f16_f32_e32 v61, v61
	v_cndmask_b32_e32 v61, 0, v61, vcc
	v_cndmask_b32_e64 v107, v61, v60, s[4:5]
	v_cvt_f16_f32_e32 v60, v58
	v_cvt_f32_f16_e32 v61, v60
	v_sub_f32_e32 v61, v58, v61
	v_cvt_f16_f32_e32 v61, v61
	v_cndmask_b32_e32 v61, 0, v61, vcc
	v_cndmask_b32_e64 v108, v61, v60, s[4:5]
	v_cvt_f16_f32_e32 v60, v59
	v_cvt_f32_f16_e32 v61, v60
	v_sub_f32_e32 v61, v59, v61
	v_cvt_f16_f32_e32 v61, v61
	v_cndmask_b32_e32 v61, 0, v61, vcc
	v_cndmask_b32_e64 v109, v61, v60, s[4:5]
	v_pack_b32_f16 v116, v94, v95
	v_pack_b32_f16 v117, v96, v97
	v_pack_b32_f16 v118, v98, v99
	v_pack_b32_f16 v119, v100, v101
	v_pack_b32_f16 v120, v102, v103
	v_pack_b32_f16 v121, v104, v105
	v_pack_b32_f16 v122, v106, v107
	v_pack_b32_f16 v123, v108, v109
	s_cmp_eq_u32 s34, 0
	s_cbranch_scc1 .Lcb_r0
	s_cmp_eq_u32 s34, 1
	s_cbranch_scc1 .Lcb_r1
	s_cmp_eq_u32 s34, 2
	s_cbranch_scc1 .Lcb_r2
	s_barrier
	ds_read_b128 v[44:47], v75 offset:0
	ds_read_b128 v[68:71], v75 offset:1024
	s_waitcnt lgkmcnt(0)
	v_mfma_f32_16x16x32_f16 v[84:87], v[2:5], v[44:47], v[18:21]
	v_mfma_f32_16x16x32_f16 v[88:91], v[14:17], v[44:47], v[38:41]
	v_mfma_f32_16x16x32_f16 v[84:87], v[6:9], v[68:71], v[84:87]
	v_mfma_f32_16x16x32_f16 v[88:91], v[10:13], v[68:71], v[88:91]
	s_barrier
	ds_read_b128 v[56:59], v75 offset:6144
	ds_read_b128 v[60:63], v75 offset:7168
	ds_read_b128 v[44:47], v75 offset:2048
	ds_read_b128 v[68:71], v75 offset:3072
	s_waitcnt lgkmcnt(3)
	v_mfma_f32_16x16x32_f16 v[84:87], v[30:33], v[56:59], v[84:87]
	v_mfma_f32_16x16x32_f16 v[88:91], v[22:25], v[56:59], v[88:91]
	s_waitcnt lgkmcnt(2)
	v_mfma_f32_16x16x32_f16 v[84:87], v[34:37], v[60:63], v[84:87]
	v_mfma_f32_16x16x32_f16 v[88:91], v[26:29], v[60:63], v[88:91]
	s_nop 7
	v_exp_f32_e32 v94, v86
	v_exp_f32_e32 v95, v90
	v_exp_f32_e32 v96, v84
	v_exp_f32_e32 v97, v88
	v_exp_f32_e32 v98, v85
	v_exp_f32_e32 v99, v89
	v_pk_add_f32 v[100:101], v[94:95], 1.0 op_sel_hi:[1,0]
	v_pk_fma_f32 v[102:103], v[94:95], s[8:9], v[92:93] op_sel_hi:[1,0,0]
	v_pk_fma_f32 v[100:101], v[96:97], v[100:101], v[100:101]
	v_pk_fma_f32 v[104:105], v[100:101], v[98:99], v[100:101]
	v_rcp_f32_e32 v104, v104
	v_rcp_f32_e32 v105, v105
	v_pk_fma_f32 v[102:103], v[102:103], v[98:99], v[102:103]
	v_pk_fma_f32 v[102:103], v[64:65], v[100:101], v[102:103]
	v_exp_f32_e32 v106, v87
	v_pk_mul_f32 v[64:65], v[102:103], v[104:105]
	v_exp_f32_e32 v108, v64
	v_exp_f32_e32 v109, v65
	v_exp_f32_e32 v107, v91
	v_pk_add_f32 v[110:111], v[108:109], 1.0 op_sel_hi:[1,0]
	v_pk_fma_f32 v[110:111], v[110:111], v[106:107], v[110:111]
	v_rcp_f32_e32 v110, v110
	v_rcp_f32_e32 v111, v111
	v_pk_add_f32 v[112:113], v[108:109], -1.0 op_sel_hi:[1,0]
	v_pk_mul_f32 v[112:113], v[112:113], v[110:111]
	v_cvt_pk_f16_f32 v114, v112, v113
	ds_write_b32 v81, v114 offset:4096
	s_waitcnt lgkmcnt(1)
	v_mfma_f32_16x16x32_f16 v[84:87], v[2:5], v[44:47], v[18:21]
	v_mfma_f32_16x16x32_f16 v[88:91], v[14:17], v[44:47], v[38:41]
	v_mfma_f32_16x16x32_f16 v[84:87], v[6:9], v[68:71], v[84:87]
	v_mfma_f32_16x16x32_f16 v[88:91], v[10:13], v[68:71], v[88:91]
	s_waitcnt lgkmcnt(0)
	s_barrier
	ds_read_b128 v[56:59], v75 offset:4096
	ds_read_b128 v[60:63], v75 offset:5120
	ds_read_b128 v[44:47], v75 offset:0
	ds_read_b128 v[68:71], v75 offset:1024
	s_waitcnt lgkmcnt(3)
	v_mfma_f32_16x16x32_f16 v[84:87], v[30:33], v[56:59], v[84:87]
	v_mfma_f32_16x16x32_f16 v[88:91], v[22:25], v[56:59], v[88:91]
	s_waitcnt lgkmcnt(2)
	v_mfma_f32_16x16x32_f16 v[84:87], v[34:37], v[60:63], v[84:87]
	v_mfma_f32_16x16x32_f16 v[88:91], v[26:29], v[60:63], v[88:91]
	s_nop 7
	v_exp_f32_e32 v94, v86
	v_exp_f32_e32 v95, v90
	v_exp_f32_e32 v96, v84
	v_exp_f32_e32 v97, v88
	v_exp_f32_e32 v98, v85
	v_exp_f32_e32 v99, v89
	v_pk_add_f32 v[100:101], v[94:95], 1.0 op_sel_hi:[1,0]
	v_pk_fma_f32 v[102:103], v[94:95], s[8:9], v[92:93] op_sel_hi:[1,0,0]
	v_pk_fma_f32 v[100:101], v[96:97], v[100:101], v[100:101]
	v_pk_fma_f32 v[104:105], v[100:101], v[98:99], v[100:101]
	v_rcp_f32_e32 v104, v104
	v_rcp_f32_e32 v105, v105
	v_pk_fma_f32 v[102:103], v[102:103], v[98:99], v[102:103]
	v_pk_fma_f32 v[102:103], v[64:65], v[100:101], v[102:103]
	v_exp_f32_e32 v106, v87
	v_pk_mul_f32 v[64:65], v[102:103], v[104:105]
	v_exp_f32_e32 v108, v64
	v_exp_f32_e32 v109, v65
	v_exp_f32_e32 v107, v91
	v_pk_add_f32 v[110:111], v[108:109], 1.0 op_sel_hi:[1,0]
	v_pk_fma_f32 v[110:111], v[110:111], v[106:107], v[110:111]
	v_rcp_f32_e32 v110, v110
	v_rcp_f32_e32 v111, v111
	v_pk_add_f32 v[112:113], v[108:109], -1.0 op_sel_hi:[1,0]
	v_pk_mul_f32 v[112:113], v[112:113], v[110:111]
	v_cvt_pk_f16_f32 v114, v112, v113
	ds_write_b32 v81, v114 offset:6144
	s_waitcnt lgkmcnt(1)
	v_mfma_f32_16x16x32_f16 v[84:87], v[2:5], v[44:47], v[18:21]
	v_mfma_f32_16x16x32_f16 v[88:91], v[14:17], v[44:47], v[38:41]
	v_mfma_f32_16x16x32_f16 v[84:87], v[6:9], v[68:71], v[84:87]
	v_mfma_f32_16x16x32_f16 v[88:91], v[10:13], v[68:71], v[88:91]
	s_waitcnt lgkmcnt(0)
	.p2align	6
.Lcb3_loop:
	s_barrier
	ds_read_b128 v[56:59], v75 offset:6144
	ds_read_b128 v[60:63], v75 offset:7168
	ds_read_b128 v[44:47], v75 offset:2048
	ds_read_b128 v[68:71], v75 offset:3072
	s_waitcnt lgkmcnt(3)
	v_mfma_f32_16x16x32_f16 v[84:87], v[30:33], v[56:59], v[84:87]
	v_mfma_f32_16x16x32_f16 v[88:91], v[22:25], v[56:59], v[88:91]
	s_waitcnt lgkmcnt(2)
	v_mfma_f32_16x16x32_f16 v[84:87], v[34:37], v[60:63], v[84:87]
	v_mfma_f32_16x16x32_f16 v[88:91], v[26:29], v[60:63], v[88:91]
	s_nop 7
	v_exp_f32_e32 v94, v86
	v_exp_f32_e32 v95, v90
	v_exp_f32_e32 v96, v84
	v_exp_f32_e32 v97, v88
	v_exp_f32_e32 v98, v85
	v_exp_f32_e32 v99, v89
	v_pk_add_f32 v[100:101], v[94:95], 1.0 op_sel_hi:[1,0]
	v_pk_fma_f32 v[102:103], v[94:95], s[8:9], v[92:93] op_sel_hi:[1,0,0]
	v_pk_fma_f32 v[100:101], v[96:97], v[100:101], v[100:101]
	v_pk_fma_f32 v[104:105], v[100:101], v[98:99], v[100:101]
	v_rcp_f32_e32 v104, v104
	v_rcp_f32_e32 v105, v105
	v_pk_fma_f32 v[102:103], v[102:103], v[98:99], v[102:103]
	v_pk_fma_f32 v[102:103], v[64:65], v[100:101], v[102:103]
	v_exp_f32_e32 v106, v87
	v_pk_mul_f32 v[64:65], v[102:103], v[104:105]
	v_exp_f32_e32 v108, v64
	v_exp_f32_e32 v109, v65
	v_exp_f32_e32 v107, v91
	v_pk_add_f32 v[110:111], v[108:109], 1.0 op_sel_hi:[1,0]
	v_pk_fma_f32 v[110:111], v[110:111], v[106:107], v[110:111]
	v_rcp_f32_e32 v110, v110
	v_rcp_f32_e32 v111, v111
	v_pk_add_f32 v[112:113], v[108:109], -1.0 op_sel_hi:[1,0]
	v_pk_mul_f32 v[112:113], v[112:113], v[110:111]
	v_cvt_pk_f16_f32 v114, v112, v113
	ds_write_b32 v81, v114 offset:4096
	s_waitcnt lgkmcnt(1)
	v_mfma_f32_16x16x32_f16 v[84:87], v[2:5], v[44:47], v[18:21]
	v_mfma_f32_16x16x32_f16 v[88:91], v[14:17], v[44:47], v[38:41]
	v_mfma_f32_16x16x32_f16 v[84:87], v[6:9], v[68:71], v[84:87]
	v_mfma_f32_16x16x32_f16 v[88:91], v[10:13], v[68:71], v[88:91]
	s_waitcnt lgkmcnt(0)
	s_barrier
	ds_read_b128 v[56:59], v75 offset:4096
	ds_read_b128 v[60:63], v75 offset:5120
	ds_read_b128 v[44:47], v75 offset:0
	ds_read_b128 v[68:71], v75 offset:1024
	s_waitcnt lgkmcnt(3)
	v_mfma_f32_16x16x32_f16 v[84:87], v[30:33], v[56:59], v[84:87]
	v_mfma_f32_16x16x32_f16 v[88:91], v[22:25], v[56:59], v[88:91]
	s_waitcnt lgkmcnt(2)
	v_mfma_f32_16x16x32_f16 v[84:87], v[34:37], v[60:63], v[84:87]
	v_mfma_f32_16x16x32_f16 v[88:91], v[26:29], v[60:63], v[88:91]
	s_nop 7
	v_exp_f32_e32 v94, v86
	v_exp_f32_e32 v95, v90
	v_exp_f32_e32 v96, v84
	v_exp_f32_e32 v97, v88
	v_exp_f32_e32 v98, v85
	v_exp_f32_e32 v99, v89
	v_pk_add_f32 v[100:101], v[94:95], 1.0 op_sel_hi:[1,0]
	v_pk_fma_f32 v[102:103], v[94:95], s[8:9], v[92:93] op_sel_hi:[1,0,0]
	v_pk_fma_f32 v[100:101], v[96:97], v[100:101], v[100:101]
	v_pk_fma_f32 v[104:105], v[100:101], v[98:99], v[100:101]
	v_rcp_f32_e32 v104, v104
	v_rcp_f32_e32 v105, v105
	v_pk_fma_f32 v[102:103], v[102:103], v[98:99], v[102:103]
	v_pk_fma_f32 v[102:103], v[64:65], v[100:101], v[102:103]
	v_exp_f32_e32 v106, v87
	v_pk_mul_f32 v[64:65], v[102:103], v[104:105]
	v_exp_f32_e32 v108, v64
	v_exp_f32_e32 v109, v65
	v_exp_f32_e32 v107, v91
	v_pk_add_f32 v[110:111], v[108:109], 1.0 op_sel_hi:[1,0]
	v_pk_fma_f32 v[110:111], v[110:111], v[106:107], v[110:111]
	v_rcp_f32_e32 v110, v110
	v_rcp_f32_e32 v111, v111
	v_pk_add_f32 v[112:113], v[108:109], -1.0 op_sel_hi:[1,0]
	v_pk_mul_f32 v[112:113], v[112:113], v[110:111]
	v_cvt_pk_f16_f32 v114, v112, v113
	ds_write_b32 v81, v114 offset:6144
	s_waitcnt lgkmcnt(1)
	v_mfma_f32_16x16x32_f16 v[84:87], v[2:5], v[44:47], v[18:21]
	v_mfma_f32_16x16x32_f16 v[88:91], v[14:17], v[44:47], v[38:41]
	v_mfma_f32_16x16x32_f16 v[84:87], v[6:9], v[68:71], v[84:87]
	v_mfma_f32_16x16x32_f16 v[88:91], v[10:13], v[68:71], v[88:91]
	s_waitcnt lgkmcnt(0)
	s_barrier
	ds_read_b128 v[56:59], v75 offset:6144
	ds_read_b128 v[60:63], v75 offset:7168
	ds_read_b128 v[44:47], v75 offset:2048
	ds_read_b128 v[68:71], v75 offset:3072
	s_waitcnt lgkmcnt(3)
	v_mfma_f32_16x16x32_f16 v[84:87], v[30:33], v[56:59], v[84:87]
	v_mfma_f32_16x16x32_f16 v[88:91], v[22:25], v[56:59], v[88:91]
	s_waitcnt lgkmcnt(2)
	v_mfma_f32_16x16x32_f16 v[84:87], v[34:37], v[60:63], v[84:87]
	v_mfma_f32_16x16x32_f16 v[88:91], v[26:29], v[60:63], v[88:91]
	s_nop 7
	v_exp_f32_e32 v94, v86
	v_exp_f32_e32 v95, v90
	v_exp_f32_e32 v96, v84
	v_exp_f32_e32 v97, v88
	v_exp_f32_e32 v98, v85
	v_exp_f32_e32 v99, v89
	v_pk_add_f32 v[100:101], v[94:95], 1.0 op_sel_hi:[1,0]
	v_pk_fma_f32 v[102:103], v[94:95], s[8:9], v[92:93] op_sel_hi:[1,0,0]
	v_pk_fma_f32 v[100:101], v[96:97], v[100:101], v[100:101]
	v_pk_fma_f32 v[104:105], v[100:101], v[98:99], v[100:101]
	v_rcp_f32_e32 v104, v104
	v_rcp_f32_e32 v105, v105
	v_pk_fma_f32 v[102:103], v[102:103], v[98:99], v[102:103]
	v_pk_fma_f32 v[102:103], v[64:65], v[100:101], v[102:103]
	v_exp_f32_e32 v106, v87
	v_pk_mul_f32 v[64:65], v[102:103], v[104:105]
	v_exp_f32_e32 v108, v64
	v_exp_f32_e32 v109, v65
	v_exp_f32_e32 v107, v91
	v_pk_add_f32 v[110:111], v[108:109], 1.0 op_sel_hi:[1,0]
	v_pk_fma_f32 v[110:111], v[110:111], v[106:107], v[110:111]
	v_rcp_f32_e32 v110, v110
	v_rcp_f32_e32 v111, v111
	v_pk_add_f32 v[112:113], v[108:109], -1.0 op_sel_hi:[1,0]
	v_pk_mul_f32 v[112:113], v[112:113], v[110:111]
	v_cvt_pk_f16_f32 v114, v112, v113
	ds_write_b32 v81, v114 offset:4096
	s_waitcnt lgkmcnt(1)
	v_mfma_f32_16x16x32_f16 v[84:87], v[2:5], v[44:47], v[18:21]
	v_mfma_f32_16x16x32_f16 v[88:91], v[14:17], v[44:47], v[38:41]
	v_mfma_f32_16x16x32_f16 v[84:87], v[6:9], v[68:71], v[84:87]
	v_mfma_f32_16x16x32_f16 v[88:91], v[10:13], v[68:71], v[88:91]
	s_waitcnt lgkmcnt(0)
	s_barrier
	ds_read_b128 v[56:59], v75 offset:4096
	ds_read_b128 v[60:63], v75 offset:5120
	ds_read_b128 v[44:47], v75 offset:0
	ds_read_b128 v[68:71], v75 offset:1024
	s_waitcnt lgkmcnt(3)
	v_mfma_f32_16x16x32_f16 v[84:87], v[30:33], v[56:59], v[84:87]
	v_mfma_f32_16x16x32_f16 v[88:91], v[22:25], v[56:59], v[88:91]
	s_waitcnt lgkmcnt(2)
	v_mfma_f32_16x16x32_f16 v[84:87], v[34:37], v[60:63], v[84:87]
	v_mfma_f32_16x16x32_f16 v[88:91], v[26:29], v[60:63], v[88:91]
	s_nop 7
	v_exp_f32_e32 v94, v86
	v_exp_f32_e32 v95, v90
	v_exp_f32_e32 v96, v84
	v_exp_f32_e32 v97, v88
	v_exp_f32_e32 v98, v85
	v_exp_f32_e32 v99, v89
	v_pk_add_f32 v[100:101], v[94:95], 1.0 op_sel_hi:[1,0]
	v_pk_fma_f32 v[102:103], v[94:95], s[8:9], v[92:93] op_sel_hi:[1,0,0]
	v_pk_fma_f32 v[100:101], v[96:97], v[100:101], v[100:101]
	v_pk_fma_f32 v[104:105], v[100:101], v[98:99], v[100:101]
	v_rcp_f32_e32 v104, v104
	v_rcp_f32_e32 v105, v105
	v_pk_fma_f32 v[102:103], v[102:103], v[98:99], v[102:103]
	v_pk_fma_f32 v[102:103], v[64:65], v[100:101], v[102:103]
	v_exp_f32_e32 v106, v87
	v_pk_mul_f32 v[64:65], v[102:103], v[104:105]
	v_exp_f32_e32 v108, v64
	v_exp_f32_e32 v109, v65
	v_exp_f32_e32 v107, v91
	v_pk_add_f32 v[110:111], v[108:109], 1.0 op_sel_hi:[1,0]
	v_pk_fma_f32 v[110:111], v[110:111], v[106:107], v[110:111]
	v_rcp_f32_e32 v110, v110
	v_rcp_f32_e32 v111, v111
	v_pk_add_f32 v[112:113], v[108:109], -1.0 op_sel_hi:[1,0]
	v_pk_mul_f32 v[112:113], v[112:113], v[110:111]
	v_cvt_pk_f16_f32 v114, v112, v113
	ds_write_b32 v81, v114 offset:6144
	s_waitcnt lgkmcnt(1)
	v_mfma_f32_16x16x32_f16 v[84:87], v[2:5], v[44:47], v[18:21]
	v_mfma_f32_16x16x32_f16 v[88:91], v[14:17], v[44:47], v[38:41]
	v_mfma_f32_16x16x32_f16 v[84:87], v[6:9], v[68:71], v[84:87]
	v_mfma_f32_16x16x32_f16 v[88:91], v[10:13], v[68:71], v[88:91]
	s_waitcnt lgkmcnt(0)
	v_min_f32_e32 v64, 0x42700000, v64
	v_min_f32_e32 v65, 0x42700000, v65
	s_add_u32 s12, s12, 4
	v_add_u32_e32 v124, 16, v124
	s_cmp_lt_u32 s12, 452
	s_cbranch_scc1 .Lcb3_loop
	s_barrier
	ds_read_b128 v[56:59], v75 offset:6144
	ds_read_b128 v[60:63], v75 offset:7168
	s_waitcnt lgkmcnt(0)
	s_waitcnt lgkmcnt(0)
	s_barrier
	s_waitcnt lgkmcnt(0)
	s_endpgm
.Lcb_r0:
	s_barrier
	ds_read_b128 v[44:47], v75 offset:0
	ds_read_b128 v[68:71], v75 offset:1024
	s_waitcnt lgkmcnt(0)
	v_mfma_f32_16x16x32_f16 v[84:87], v[2:5], v[44:47], v[18:21]
	v_mfma_f32_16x16x32_f16 v[88:91], v[14:17], v[44:47], v[38:41]
	v_mfma_f32_16x16x32_f16 v[84:87], v[6:9], v[68:71], v[84:87]
	v_mfma_f32_16x16x32_f16 v[88:91], v[10:13], v[68:71], v[88:91]
	s_barrier
	ds_read_b128 v[56:59], v75 offset:6144
	ds_read_b128 v[60:63], v75 offset:7168
	ds_read_b128 v[44:47], v75 offset:2048
	ds_read_b128 v[68:71], v75 offset:3072
	s_waitcnt lgkmcnt(3)
	v_mfma_f32_16x16x32_f16 v[84:87], v[30:33], v[56:59], v[84:87]
	v_mfma_f32_16x16x32_f16 v[88:91], v[22:25], v[56:59], v[88:91]
	s_waitcnt lgkmcnt(2)
	v_mfma_f32_16x16x32_f16 v[84:87], v[34:37], v[60:63], v[84:87]
	v_mfma_f32_16x16x32_f16 v[88:91], v[26:29], v[60:63], v[88:91]
	s_nop 7
	v_exp_f32_e32 v94, v86
	v_exp_f32_e32 v95, v90
	v_exp_f32_e32 v96, v84
	v_exp_f32_e32 v97, v88
	v_exp_f32_e32 v98, v85
	v_exp_f32_e32 v99, v89
	v_pk_add_f32 v[100:101], v[94:95], 1.0 op_sel_hi:[1,0]
	v_pk_fma_f32 v[102:103], v[94:95], s[8:9], v[92:93] op_sel_hi:[1,0,0]
	v_pk_fma_f32 v[100:101], v[96:97], v[100:101], v[100:101]
	v_pk_fma_f32 v[104:105], v[100:101], v[98:99], v[100:101]
	v_rcp_f32_e32 v104, v104
	v_rcp_f32_e32 v105, v105
	v_pk_fma_f32 v[102:103], v[102:103], v[98:99], v[102:103]
	v_pk_fma_f32 v[102:103], v[64:65], v[100:101], v[102:103]
	v_exp_f32_e32 v106, v87
	v_pk_mul_f32 v[64:65], v[102:103], v[104:105]
	v_exp_f32_e32 v108, v64
	v_exp_f32_e32 v109, v65
	v_exp_f32_e32 v107, v91
	v_pk_add_f32 v[110:111], v[108:109], 1.0 op_sel_hi:[1,0]
	v_pk_fma_f32 v[110:111], v[110:111], v[106:107], v[110:111]
	v_rcp_f32_e32 v110, v110
	v_rcp_f32_e32 v111, v111
	v_pk_add_f32 v[112:113], v[108:109], -1.0 op_sel_hi:[1,0]
	v_pk_mul_f32 v[112:113], v[112:113], v[110:111]
	v_cvt_pk_f16_f32 v114, v112, v113
	ds_write_b32 v81, v114 offset:4096
	s_waitcnt lgkmcnt(1)
	v_mfma_f32_16x16x32_f16 v[84:87], v[2:5], v[44:47], v[18:21]
	v_mfma_f32_16x16x32_f16 v[88:91], v[14:17], v[44:47], v[38:41]
	v_mfma_f32_16x16x32_f16 v[84:87], v[6:9], v[68:71], v[84:87]
	v_mfma_f32_16x16x32_f16 v[88:91], v[10:13], v[68:71], v[88:91]
	s_waitcnt lgkmcnt(0)
	s_barrier
	ds_read_b128 v[56:59], v75 offset:4096
	ds_read_b128 v[60:63], v75 offset:5120
	ds_read_b128 v[44:47], v75 offset:0
	ds_read_b128 v[68:71], v75 offset:1024
	s_waitcnt lgkmcnt(3)
	v_mfma_f32_16x16x32_f16 v[84:87], v[30:33], v[56:59], v[84:87]
	v_mfma_f32_16x16x32_f16 v[88:91], v[22:25], v[56:59], v[88:91]
	s_waitcnt lgkmcnt(2)
	v_mfma_f32_16x16x32_f16 v[84:87], v[34:37], v[60:63], v[84:87]
	v_mfma_f32_16x16x32_f16 v[88:91], v[26:29], v[60:63], v[88:91]
	v_mfma_f32_16x16x32_f16 v[50:53], v[116:119], v[56:59], 0
	s_nop 7
	v_exp_f32_e32 v94, v86
	v_exp_f32_e32 v95, v90
	v_exp_f32_e32 v96, v84
	v_exp_f32_e32 v97, v88
	v_exp_f32_e32 v98, v85
	v_exp_f32_e32 v99, v89
	v_add_f32_e32 v125, v50, v51
	v_add_f32_e32 v125, s28, v125
	s_mov_b64 s[16:17], exec
	s_mov_b64 exec, s[30:31]
	ds_write_b32 v74, v125 offset:128
	s_mov_b64 exec, s[16:17]
	v_pk_add_f32 v[100:101], v[94:95], 1.0 op_sel_hi:[1,0]
	v_pk_fma_f32 v[102:103], v[94:95], s[8:9], v[92:93] op_sel_hi:[1,0,0]
	v_pk_fma_f32 v[100:101], v[96:97], v[100:101], v[100:101]
	v_pk_fma_f32 v[104:105], v[100:101], v[98:99], v[100:101]
	v_rcp_f32_e32 v104, v104
	v_rcp_f32_e32 v105, v105
	v_pk_fma_f32 v[102:103], v[102:103], v[98:99], v[102:103]
	v_pk_fma_f32 v[102:103], v[64:65], v[100:101], v[102:103]
	v_exp_f32_e32 v106, v87
	v_pk_mul_f32 v[64:65], v[102:103], v[104:105]
	v_exp_f32_e32 v108, v64
	v_exp_f32_e32 v109, v65
	v_exp_f32_e32 v107, v91
	v_pk_add_f32 v[110:111], v[108:109], 1.0 op_sel_hi:[1,0]
	v_pk_fma_f32 v[110:111], v[110:111], v[106:107], v[110:111]
	v_rcp_f32_e32 v110, v110
	v_rcp_f32_e32 v111, v111
	v_pk_add_f32 v[112:113], v[108:109], -1.0 op_sel_hi:[1,0]
	v_pk_mul_f32 v[112:113], v[112:113], v[110:111]
	v_cvt_pk_f16_f32 v114, v112, v113
	ds_write_b32 v81, v114 offset:6144
	s_waitcnt lgkmcnt(1)
	v_mfma_f32_16x16x32_f16 v[84:87], v[2:5], v[44:47], v[18:21]
	v_mfma_f32_16x16x32_f16 v[88:91], v[14:17], v[44:47], v[38:41]
	v_mfma_f32_16x16x32_f16 v[84:87], v[6:9], v[68:71], v[84:87]
	v_mfma_f32_16x16x32_f16 v[88:91], v[10:13], v[68:71], v[88:91]
	s_waitcnt lgkmcnt(0)
	.p2align	6
.Lcb0_loop:
	s_barrier
	ds_read_b128 v[56:59], v75 offset:6144
	ds_read_b128 v[60:63], v75 offset:7168
	ds_read_b128 v[44:47], v75 offset:2048
	ds_read_b128 v[68:71], v75 offset:3072
	s_waitcnt lgkmcnt(3)
	v_mfma_f32_16x16x32_f16 v[84:87], v[30:33], v[56:59], v[84:87]
	v_mfma_f32_16x16x32_f16 v[88:91], v[22:25], v[56:59], v[88:91]
	s_waitcnt lgkmcnt(2)
	v_mfma_f32_16x16x32_f16 v[84:87], v[34:37], v[60:63], v[84:87]
	v_mfma_f32_16x16x32_f16 v[88:91], v[26:29], v[60:63], v[88:91]
	v_mfma_f32_16x16x32_f16 v[50:53], v[116:119], v[56:59], 0
	s_nop 7
	v_exp_f32_e32 v94, v86
	v_exp_f32_e32 v95, v90
	v_exp_f32_e32 v96, v84
	v_exp_f32_e32 v97, v88
	v_exp_f32_e32 v98, v85
	v_exp_f32_e32 v99, v89
	v_add_f32_e32 v125, v50, v51
	v_add_f32_e32 v125, s28, v125
	s_mov_b64 s[16:17], exec
	s_mov_b64 exec, s[30:31]
	ds_write_b32 v74, v125 offset:0
	s_mov_b64 exec, s[16:17]
	v_pk_add_f32 v[100:101], v[94:95], 1.0 op_sel_hi:[1,0]
	v_pk_fma_f32 v[102:103], v[94:95], s[8:9], v[92:93] op_sel_hi:[1,0,0]
	v_pk_fma_f32 v[100:101], v[96:97], v[100:101], v[100:101]
	v_pk_fma_f32 v[104:105], v[100:101], v[98:99], v[100:101]
	v_rcp_f32_e32 v104, v104
	v_rcp_f32_e32 v105, v105
	v_pk_fma_f32 v[102:103], v[102:103], v[98:99], v[102:103]
	v_pk_fma_f32 v[102:103], v[64:65], v[100:101], v[102:103]
	v_exp_f32_e32 v106, v87
	v_pk_mul_f32 v[64:65], v[102:103], v[104:105]
	v_exp_f32_e32 v108, v64
	v_exp_f32_e32 v109, v65
	v_exp_f32_e32 v107, v91
	v_pk_add_f32 v[110:111], v[108:109], 1.0 op_sel_hi:[1,0]
	v_pk_fma_f32 v[110:111], v[110:111], v[106:107], v[110:111]
	v_rcp_f32_e32 v110, v110
	v_rcp_f32_e32 v111, v111
	v_pk_add_f32 v[112:113], v[108:109], -1.0 op_sel_hi:[1,0]
	v_pk_mul_f32 v[112:113], v[112:113], v[110:111]
	v_cvt_pk_f16_f32 v114, v112, v113
	ds_write_b32 v81, v114 offset:4096
	s_waitcnt lgkmcnt(1)
	v_mfma_f32_16x16x32_f16 v[84:87], v[2:5], v[44:47], v[18:21]
	v_mfma_f32_16x16x32_f16 v[88:91], v[14:17], v[44:47], v[38:41]
	v_mfma_f32_16x16x32_f16 v[84:87], v[6:9], v[68:71], v[84:87]
	v_mfma_f32_16x16x32_f16 v[88:91], v[10:13], v[68:71], v[88:91]
	s_waitcnt lgkmcnt(0)
	s_barrier
	ds_read_b128 v[56:59], v75 offset:4096
	ds_read_b128 v[60:63], v75 offset:5120
	ds_read_b128 v[44:47], v75 offset:0
	ds_read_b128 v[68:71], v75 offset:1024
	s_waitcnt lgkmcnt(3)
	v_mfma_f32_16x16x32_f16 v[84:87], v[30:33], v[56:59], v[84:87]
	v_mfma_f32_16x16x32_f16 v[88:91], v[22:25], v[56:59], v[88:91]
	s_waitcnt lgkmcnt(2)
	v_mfma_f32_16x16x32_f16 v[84:87], v[34:37], v[60:63], v[84:87]
	v_mfma_f32_16x16x32_f16 v[88:91], v[26:29], v[60:63], v[88:91]
	v_mfma_f32_16x16x32_f16 v[50:53], v[116:119], v[56:59], 0
	s_nop 7
	v_exp_f32_e32 v94, v86
	v_exp_f32_e32 v95, v90
	v_exp_f32_e32 v96, v84
	v_exp_f32_e32 v97, v88
	v_exp_f32_e32 v98, v85
	v_exp_f32_e32 v99, v89
	v_add_f32_e32 v125, v50, v51
	v_add_f32_e32 v125, s28, v125
	s_mov_b64 s[16:17], exec
	s_mov_b64 exec, s[30:31]
	ds_write_b32 v74, v125 offset:128
	s_mov_b64 exec, s[16:17]
	v_pk_add_f32 v[100:101], v[94:95], 1.0 op_sel_hi:[1,0]
	v_pk_fma_f32 v[102:103], v[94:95], s[8:9], v[92:93] op_sel_hi:[1,0,0]
	v_pk_fma_f32 v[100:101], v[96:97], v[100:101], v[100:101]
	v_pk_fma_f32 v[104:105], v[100:101], v[98:99], v[100:101]
	v_rcp_f32_e32 v104, v104
	v_rcp_f32_e32 v105, v105
	v_pk_fma_f32 v[102:103], v[102:103], v[98:99], v[102:103]
	v_pk_fma_f32 v[102:103], v[64:65], v[100:101], v[102:103]
	v_exp_f32_e32 v106, v87
	v_pk_mul_f32 v[64:65], v[102:103], v[104:105]
	v_exp_f32_e32 v108, v64
	v_exp_f32_e32 v109, v65
	v_exp_f32_e32 v107, v91
	v_pk_add_f32 v[110:111], v[108:109], 1.0 op_sel_hi:[1,0]
	v_pk_fma_f32 v[110:111], v[110:111], v[106:107], v[110:111]
	v_rcp_f32_e32 v110, v110
	v_rcp_f32_e32 v111, v111
	v_pk_add_f32 v[112:113], v[108:109], -1.0 op_sel_hi:[1,0]
	v_pk_mul_f32 v[112:113], v[112:113], v[110:111]
	v_cvt_pk_f16_f32 v114, v112, v113
	ds_write_b32 v81, v114 offset:6144
	s_waitcnt lgkmcnt(1)
	v_mfma_f32_16x16x32_f16 v[84:87], v[2:5], v[44:47], v[18:21]
	v_mfma_f32_16x16x32_f16 v[88:91], v[14:17], v[44:47], v[38:41]
	v_mfma_f32_16x16x32_f16 v[84:87], v[6:9], v[68:71], v[84:87]
	v_mfma_f32_16x16x32_f16 v[88:91], v[10:13], v[68:71], v[88:91]
	s_waitcnt lgkmcnt(0)
	s_barrier
	ds_read_b128 v[56:59], v75 offset:6144
	ds_read_b128 v[60:63], v75 offset:7168
	ds_read_b128 v[44:47], v75 offset:2048
	ds_read_b128 v[68:71], v75 offset:3072
	s_waitcnt lgkmcnt(3)
	v_mfma_f32_16x16x32_f16 v[84:87], v[30:33], v[56:59], v[84:87]
	v_mfma_f32_16x16x32_f16 v[88:91], v[22:25], v[56:59], v[88:91]
	s_waitcnt lgkmcnt(2)
	v_mfma_f32_16x16x32_f16 v[84:87], v[34:37], v[60:63], v[84:87]
	v_mfma_f32_16x16x32_f16 v[88:91], v[26:29], v[60:63], v[88:91]
	v_mfma_f32_16x16x32_f16 v[50:53], v[116:119], v[56:59], 0
	s_nop 7
	v_exp_f32_e32 v94, v86
	v_exp_f32_e32 v95, v90
	v_exp_f32_e32 v96, v84
	v_exp_f32_e32 v97, v88
	v_exp_f32_e32 v98, v85
	v_exp_f32_e32 v99, v89
	v_add_f32_e32 v125, v50, v51
	v_add_f32_e32 v125, s28, v125
	s_mov_b64 s[16:17], exec
	s_mov_b64 exec, s[30:31]
	ds_write_b32 v74, v125 offset:0
	s_mov_b64 exec, s[16:17]
	v_pk_add_f32 v[100:101], v[94:95], 1.0 op_sel_hi:[1,0]
	v_pk_fma_f32 v[102:103], v[94:95], s[8:9], v[92:93] op_sel_hi:[1,0,0]
	v_pk_fma_f32 v[100:101], v[96:97], v[100:101], v[100:101]
	v_pk_fma_f32 v[104:105], v[100:101], v[98:99], v[100:101]
	v_rcp_f32_e32 v104, v104
	v_rcp_f32_e32 v105, v105
	v_pk_fma_f32 v[102:103], v[102:103], v[98:99], v[102:103]
	v_pk_fma_f32 v[102:103], v[64:65], v[100:101], v[102:103]
	v_exp_f32_e32 v106, v87
	v_pk_mul_f32 v[64:65], v[102:103], v[104:105]
	v_exp_f32_e32 v108, v64
	v_exp_f32_e32 v109, v65
	v_exp_f32_e32 v107, v91
	v_pk_add_f32 v[110:111], v[108:109], 1.0 op_sel_hi:[1,0]
	v_pk_fma_f32 v[110:111], v[110:111], v[106:107], v[110:111]
	v_rcp_f32_e32 v110, v110
	v_rcp_f32_e32 v111, v111
	v_pk_add_f32 v[112:113], v[108:109], -1.0 op_sel_hi:[1,0]
	v_pk_mul_f32 v[112:113], v[112:113], v[110:111]
	v_cvt_pk_f16_f32 v114, v112, v113
	ds_write_b32 v81, v114 offset:4096
	s_waitcnt lgkmcnt(1)
	v_mfma_f32_16x16x32_f16 v[84:87], v[2:5], v[44:47], v[18:21]
	v_mfma_f32_16x16x32_f16 v[88:91], v[14:17], v[44:47], v[38:41]
	v_mfma_f32_16x16x32_f16 v[84:87], v[6:9], v[68:71], v[84:87]
	v_mfma_f32_16x16x32_f16 v[88:91], v[10:13], v[68:71], v[88:91]
	s_waitcnt lgkmcnt(0)
	s_barrier
	ds_read_b128 v[56:59], v75 offset:4096
	ds_read_b128 v[60:63], v75 offset:5120
	ds_read_b128 v[44:47], v75 offset:0
	ds_read_b128 v[68:71], v75 offset:1024
	s_waitcnt lgkmcnt(3)
	v_mfma_f32_16x16x32_f16 v[84:87], v[30:33], v[56:59], v[84:87]
	v_mfma_f32_16x16x32_f16 v[88:91], v[22:25], v[56:59], v[88:91]
	s_waitcnt lgkmcnt(2)
	v_mfma_f32_16x16x32_f16 v[84:87], v[34:37], v[60:63], v[84:87]
	v_mfma_f32_16x16x32_f16 v[88:91], v[26:29], v[60:63], v[88:91]
	v_mfma_f32_16x16x32_f16 v[50:53], v[116:119], v[56:59], 0
	s_nop 7
	v_exp_f32_e32 v94, v86
	v_exp_f32_e32 v95, v90
	v_exp_f32_e32 v96, v84
	v_exp_f32_e32 v97, v88
	v_exp_f32_e32 v98, v85
	v_exp_f32_e32 v99, v89
	v_add_f32_e32 v125, v50, v51
	v_add_f32_e32 v125, s28, v125
	s_mov_b64 s[16:17], exec
	s_mov_b64 exec, s[30:31]
	ds_write_b32 v74, v125 offset:128
	s_mov_b64 exec, s[16:17]
	v_pk_add_f32 v[100:101], v[94:95], 1.0 op_sel_hi:[1,0]
	v_pk_fma_f32 v[102:103], v[94:95], s[8:9], v[92:93] op_sel_hi:[1,0,0]
	v_pk_fma_f32 v[100:101], v[96:97], v[100:101], v[100:101]
	v_pk_fma_f32 v[104:105], v[100:101], v[98:99], v[100:101]
	v_rcp_f32_e32 v104, v104
	v_rcp_f32_e32 v105, v105
	v_pk_fma_f32 v[102:103], v[102:103], v[98:99], v[102:103]
	v_pk_fma_f32 v[102:103], v[64:65], v[100:101], v[102:103]
	v_exp_f32_e32 v106, v87
	v_pk_mul_f32 v[64:65], v[102:103], v[104:105]
	v_exp_f32_e32 v108, v64
	v_exp_f32_e32 v109, v65
	v_exp_f32_e32 v107, v91
	v_pk_add_f32 v[110:111], v[108:109], 1.0 op_sel_hi:[1,0]
	v_pk_fma_f32 v[110:111], v[110:111], v[106:107], v[110:111]
	v_rcp_f32_e32 v110, v110
	v_rcp_f32_e32 v111, v111
	v_pk_add_f32 v[112:113], v[108:109], -1.0 op_sel_hi:[1,0]
	v_pk_mul_f32 v[112:113], v[112:113], v[110:111]
	v_cvt_pk_f16_f32 v114, v112, v113
	ds_write_b32 v81, v114 offset:6144
	s_waitcnt lgkmcnt(1)
	v_mfma_f32_16x16x32_f16 v[84:87], v[2:5], v[44:47], v[18:21]
	v_mfma_f32_16x16x32_f16 v[88:91], v[14:17], v[44:47], v[38:41]
	v_mfma_f32_16x16x32_f16 v[84:87], v[6:9], v[68:71], v[84:87]
	v_mfma_f32_16x16x32_f16 v[88:91], v[10:13], v[68:71], v[88:91]
	s_waitcnt lgkmcnt(0)
	v_min_f32_e32 v64, 0x42700000, v64
	v_min_f32_e32 v65, 0x42700000, v65
	s_add_u32 s12, s12, 4
	v_add_u32_e32 v124, 16, v124
	s_cmp_lt_u32 s12, 452
	s_cbranch_scc1 .Lcb0_loop
	s_barrier
	ds_read_b128 v[56:59], v75 offset:6144
	ds_read_b128 v[60:63], v75 offset:7168
	s_waitcnt lgkmcnt(0)
	v_mfma_f32_16x16x32_f16 v[50:53], v[116:119], v[56:59], 0
	s_nop 7
	v_add_f32_e32 v125, v50, v51
	v_add_f32_e32 v125, s28, v125
	s_mov_b64 s[16:17], exec
	s_mov_b64 exec, s[30:31]
	ds_write_b32 v74, v125 offset:0
	s_mov_b64 exec, s[16:17]
	s_waitcnt lgkmcnt(0)
	s_barrier
	s_waitcnt lgkmcnt(0)
	s_endpgm
.Lcb_r1:
	s_barrier
	ds_read_b128 v[44:47], v75 offset:0
	ds_read_b128 v[68:71], v75 offset:1024
	s_waitcnt lgkmcnt(0)
	v_mfma_f32_16x16x32_f16 v[84:87], v[2:5], v[44:47], v[18:21]
	v_mfma_f32_16x16x32_f16 v[88:91], v[14:17], v[44:47], v[38:41]
	v_mfma_f32_16x16x32_f16 v[84:87], v[6:9], v[68:71], v[84:87]
	v_mfma_f32_16x16x32_f16 v[88:91], v[10:13], v[68:71], v[88:91]
	s_barrier
	ds_read_b128 v[56:59], v75 offset:6144
	ds_read_b128 v[60:63], v75 offset:7168
	ds_read_b128 v[44:47], v75 offset:2048
	ds_read_b128 v[68:71], v75 offset:3072
	s_waitcnt lgkmcnt(3)
	v_mfma_f32_16x16x32_f16 v[84:87], v[30:33], v[56:59], v[84:87]
	v_mfma_f32_16x16x32_f16 v[88:91], v[22:25], v[56:59], v[88:91]
	s_waitcnt lgkmcnt(2)
	v_mfma_f32_16x16x32_f16 v[84:87], v[34:37], v[60:63], v[84:87]
	v_mfma_f32_16x16x32_f16 v[88:91], v[26:29], v[60:63], v[88:91]
	s_nop 7
	v_exp_f32_e32 v94, v86
	v_exp_f32_e32 v95, v90
	v_exp_f32_e32 v96, v84
	v_exp_f32_e32 v97, v88
	v_exp_f32_e32 v98, v85
	v_exp_f32_e32 v99, v89
	v_pk_add_f32 v[100:101], v[94:95], 1.0 op_sel_hi:[1,0]
	v_pk_fma_f32 v[102:103], v[94:95], s[8:9], v[92:93] op_sel_hi:[1,0,0]
	v_pk_fma_f32 v[100:101], v[96:97], v[100:101], v[100:101]
	v_pk_fma_f32 v[104:105], v[100:101], v[98:99], v[100:101]
	v_rcp_f32_e32 v104, v104
	v_rcp_f32_e32 v105, v105
	v_pk_fma_f32 v[102:103], v[102:103], v[98:99], v[102:103]
	v_pk_fma_f32 v[102:103], v[64:65], v[100:101], v[102:103]
	v_exp_f32_e32 v106, v87
	v_pk_mul_f32 v[64:65], v[102:103], v[104:105]
	v_exp_f32_e32 v108, v64
	v_exp_f32_e32 v109, v65
	v_exp_f32_e32 v107, v91
	v_pk_add_f32 v[110:111], v[108:109], 1.0 op_sel_hi:[1,0]
	v_pk_fma_f32 v[110:111], v[110:111], v[106:107], v[110:111]
	v_rcp_f32_e32 v110, v110
	v_rcp_f32_e32 v111, v111
	v_pk_add_f32 v[112:113], v[108:109], -1.0 op_sel_hi:[1,0]
	v_pk_mul_f32 v[112:113], v[112:113], v[110:111]
	v_cvt_pk_f16_f32 v114, v112, v113
	ds_write_b32 v81, v114 offset:4096
	s_waitcnt lgkmcnt(1)
	v_mfma_f32_16x16x32_f16 v[84:87], v[2:5], v[44:47], v[18:21]
	v_mfma_f32_16x16x32_f16 v[88:91], v[14:17], v[44:47], v[38:41]
	v_mfma_f32_16x16x32_f16 v[84:87], v[6:9], v[68:71], v[84:87]
	v_mfma_f32_16x16x32_f16 v[88:91], v[10:13], v[68:71], v[88:91]
	s_waitcnt lgkmcnt(0)
	s_barrier
	ds_read_b128 v[56:59], v75 offset:4096
	ds_read_b128 v[60:63], v75 offset:5120
	ds_read_b128 v[44:47], v75 offset:0
	ds_read_b128 v[68:71], v75 offset:1024
	s_waitcnt lgkmcnt(3)
	v_mfma_f32_16x16x32_f16 v[84:87], v[30:33], v[56:59], v[84:87]
	v_mfma_f32_16x16x32_f16 v[88:91], v[22:25], v[56:59], v[88:91]
	s_waitcnt lgkmcnt(2)
	v_mfma_f32_16x16x32_f16 v[84:87], v[34:37], v[60:63], v[84:87]
	v_mfma_f32_16x16x32_f16 v[88:91], v[26:29], v[60:63], v[88:91]
	v_mfma_f32_16x16x32_f16 v[50:53], v[120:123], v[60:63], 0
	s_nop 7
	v_exp_f32_e32 v94, v86
	v_exp_f32_e32 v95, v90
	v_exp_f32_e32 v96, v84
	v_exp_f32_e32 v97, v88
	v_exp_f32_e32 v98, v85
	v_exp_f32_e32 v99, v89
	v_add_f32_e32 v125, v50, v51
	s_mov_b64 s[16:17], exec
	s_mov_b64 exec, s[30:31]
	ds_write_b32 v74, v125 offset:192
	s_mov_b64 exec, s[16:17]
	v_pk_add_f32 v[100:101], v[94:95], 1.0 op_sel_hi:[1,0]
	v_pk_fma_f32 v[102:103], v[94:95], s[8:9], v[92:93] op_sel_hi:[1,0,0]
	v_pk_fma_f32 v[100:101], v[96:97], v[100:101], v[100:101]
	v_pk_fma_f32 v[104:105], v[100:101], v[98:99], v[100:101]
	v_rcp_f32_e32 v104, v104
	v_rcp_f32_e32 v105, v105
	v_pk_fma_f32 v[102:103], v[102:103], v[98:99], v[102:103]
	v_pk_fma_f32 v[102:103], v[64:65], v[100:101], v[102:103]
	v_exp_f32_e32 v106, v87
	v_pk_mul_f32 v[64:65], v[102:103], v[104:105]
	v_exp_f32_e32 v108, v64
	v_exp_f32_e32 v109, v65
	v_exp_f32_e32 v107, v91
	v_pk_add_f32 v[110:111], v[108:109], 1.0 op_sel_hi:[1,0]
	v_pk_fma_f32 v[110:111], v[110:111], v[106:107], v[110:111]
	v_rcp_f32_e32 v110, v110
	v_rcp_f32_e32 v111, v111
	v_pk_add_f32 v[112:113], v[108:109], -1.0 op_sel_hi:[1,0]
	v_pk_mul_f32 v[112:113], v[112:113], v[110:111]
	v_cvt_pk_f16_f32 v114, v112, v113
	ds_write_b32 v81, v114 offset:6144
	s_waitcnt lgkmcnt(1)
	v_mfma_f32_16x16x32_f16 v[84:87], v[2:5], v[44:47], v[18:21]
	v_mfma_f32_16x16x32_f16 v[88:91], v[14:17], v[44:47], v[38:41]
	v_mfma_f32_16x16x32_f16 v[84:87], v[6:9], v[68:71], v[84:87]
	v_mfma_f32_16x16x32_f16 v[88:91], v[10:13], v[68:71], v[88:91]
	s_waitcnt lgkmcnt(0)
	.p2align	6
.Lcb1_loop:
	s_barrier
	ds_read_b128 v[56:59], v75 offset:6144
	ds_read_b128 v[60:63], v75 offset:7168
	ds_read_b128 v[44:47], v75 offset:2048
	ds_read_b128 v[68:71], v75 offset:3072
	s_waitcnt lgkmcnt(3)
	v_mfma_f32_16x16x32_f16 v[84:87], v[30:33], v[56:59], v[84:87]
	v_mfma_f32_16x16x32_f16 v[88:91], v[22:25], v[56:59], v[88:91]
	s_waitcnt lgkmcnt(2)
	v_mfma_f32_16x16x32_f16 v[84:87], v[34:37], v[60:63], v[84:87]
	v_mfma_f32_16x16x32_f16 v[88:91], v[26:29], v[60:63], v[88:91]
	v_mfma_f32_16x16x32_f16 v[50:53], v[120:123], v[60:63], 0
	s_nop 7
	v_exp_f32_e32 v94, v86
	v_exp_f32_e32 v95, v90
	v_exp_f32_e32 v96, v84
	v_exp_f32_e32 v97, v88
	v_exp_f32_e32 v98, v85
	v_exp_f32_e32 v99, v89
	v_add_f32_e32 v125, v50, v51
	s_mov_b64 s[16:17], exec
	s_mov_b64 exec, s[30:31]
	ds_write_b32 v74, v125 offset:64
	s_mov_b64 exec, s[16:17]
	v_pk_add_f32 v[100:101], v[94:95], 1.0 op_sel_hi:[1,0]
	v_pk_fma_f32 v[102:103], v[94:95], s[8:9], v[92:93] op_sel_hi:[1,0,0]
	v_pk_fma_f32 v[100:101], v[96:97], v[100:101], v[100:101]
	v_pk_fma_f32 v[104:105], v[100:101], v[98:99], v[100:101]
	v_rcp_f32_e32 v104, v104
	v_rcp_f32_e32 v105, v105
	v_pk_fma_f32 v[102:103], v[102:103], v[98:99], v[102:103]
	v_pk_fma_f32 v[102:103], v[64:65], v[100:101], v[102:103]
	v_exp_f32_e32 v106, v87
	v_pk_mul_f32 v[64:65], v[102:103], v[104:105]
	v_exp_f32_e32 v108, v64
	v_exp_f32_e32 v109, v65
	v_exp_f32_e32 v107, v91
	v_pk_add_f32 v[110:111], v[108:109], 1.0 op_sel_hi:[1,0]
	v_pk_fma_f32 v[110:111], v[110:111], v[106:107], v[110:111]
	v_rcp_f32_e32 v110, v110
	v_rcp_f32_e32 v111, v111
	v_pk_add_f32 v[112:113], v[108:109], -1.0 op_sel_hi:[1,0]
	v_pk_mul_f32 v[112:113], v[112:113], v[110:111]
	v_cvt_pk_f16_f32 v114, v112, v113
	ds_write_b32 v81, v114 offset:4096
	s_waitcnt lgkmcnt(1)
	v_mfma_f32_16x16x32_f16 v[84:87], v[2:5], v[44:47], v[18:21]
	v_mfma_f32_16x16x32_f16 v[88:91], v[14:17], v[44:47], v[38:41]
	v_mfma_f32_16x16x32_f16 v[84:87], v[6:9], v[68:71], v[84:87]
	v_mfma_f32_16x16x32_f16 v[88:91], v[10:13], v[68:71], v[88:91]
	s_waitcnt lgkmcnt(0)
	s_barrier
	ds_read_b128 v[56:59], v75 offset:4096
	ds_read_b128 v[60:63], v75 offset:5120
	ds_read_b128 v[44:47], v75 offset:0
	ds_read_b128 v[68:71], v75 offset:1024
	s_waitcnt lgkmcnt(3)
	v_mfma_f32_16x16x32_f16 v[84:87], v[30:33], v[56:59], v[84:87]
	v_mfma_f32_16x16x32_f16 v[88:91], v[22:25], v[56:59], v[88:91]
	s_waitcnt lgkmcnt(2)
	v_mfma_f32_16x16x32_f16 v[84:87], v[34:37], v[60:63], v[84:87]
	v_mfma_f32_16x16x32_f16 v[88:91], v[26:29], v[60:63], v[88:91]
	v_mfma_f32_16x16x32_f16 v[50:53], v[120:123], v[60:63], 0
	s_nop 7
	v_exp_f32_e32 v94, v86
	v_exp_f32_e32 v95, v90
	v_exp_f32_e32 v96, v84
	v_exp_f32_e32 v97, v88
	v_exp_f32_e32 v98, v85
	v_exp_f32_e32 v99, v89
	v_add_f32_e32 v125, v50, v51
	s_mov_b64 s[16:17], exec
	s_mov_b64 exec, s[30:31]
	ds_write_b32 v74, v125 offset:192
	s_mov_b64 exec, s[16:17]
	v_pk_add_f32 v[100:101], v[94:95], 1.0 op_sel_hi:[1,0]
	v_pk_fma_f32 v[102:103], v[94:95], s[8:9], v[92:93] op_sel_hi:[1,0,0]
	v_pk_fma_f32 v[100:101], v[96:97], v[100:101], v[100:101]
	v_pk_fma_f32 v[104:105], v[100:101], v[98:99], v[100:101]
	v_rcp_f32_e32 v104, v104
	v_rcp_f32_e32 v105, v105
	v_pk_fma_f32 v[102:103], v[102:103], v[98:99], v[102:103]
	v_pk_fma_f32 v[102:103], v[64:65], v[100:101], v[102:103]
	v_exp_f32_e32 v106, v87
	v_pk_mul_f32 v[64:65], v[102:103], v[104:105]
	v_exp_f32_e32 v108, v64
	v_exp_f32_e32 v109, v65
	v_exp_f32_e32 v107, v91
	v_pk_add_f32 v[110:111], v[108:109], 1.0 op_sel_hi:[1,0]
	v_pk_fma_f32 v[110:111], v[110:111], v[106:107], v[110:111]
	v_rcp_f32_e32 v110, v110
	v_rcp_f32_e32 v111, v111
	v_pk_add_f32 v[112:113], v[108:109], -1.0 op_sel_hi:[1,0]
	v_pk_mul_f32 v[112:113], v[112:113], v[110:111]
	v_cvt_pk_f16_f32 v114, v112, v113
	ds_write_b32 v81, v114 offset:6144
	s_waitcnt lgkmcnt(1)
	v_mfma_f32_16x16x32_f16 v[84:87], v[2:5], v[44:47], v[18:21]
	v_mfma_f32_16x16x32_f16 v[88:91], v[14:17], v[44:47], v[38:41]
	v_mfma_f32_16x16x32_f16 v[84:87], v[6:9], v[68:71], v[84:87]
	v_mfma_f32_16x16x32_f16 v[88:91], v[10:13], v[68:71], v[88:91]
	s_waitcnt lgkmcnt(0)
	s_barrier
	ds_read_b128 v[56:59], v75 offset:6144
	ds_read_b128 v[60:63], v75 offset:7168
	ds_read_b128 v[44:47], v75 offset:2048
	ds_read_b128 v[68:71], v75 offset:3072
	s_waitcnt lgkmcnt(3)
	v_mfma_f32_16x16x32_f16 v[84:87], v[30:33], v[56:59], v[84:87]
	v_mfma_f32_16x16x32_f16 v[88:91], v[22:25], v[56:59], v[88:91]
	s_waitcnt lgkmcnt(2)
	v_mfma_f32_16x16x32_f16 v[84:87], v[34:37], v[60:63], v[84:87]
	v_mfma_f32_16x16x32_f16 v[88:91], v[26:29], v[60:63], v[88:91]
	v_mfma_f32_16x16x32_f16 v[50:53], v[120:123], v[60:63], 0
	s_nop 7
	v_exp_f32_e32 v94, v86
	v_exp_f32_e32 v95, v90
	v_exp_f32_e32 v96, v84
	v_exp_f32_e32 v97, v88
	v_exp_f32_e32 v98, v85
	v_exp_f32_e32 v99, v89
	v_add_f32_e32 v125, v50, v51
	s_mov_b64 s[16:17], exec
	s_mov_b64 exec, s[30:31]
	ds_write_b32 v74, v125 offset:64
	s_mov_b64 exec, s[16:17]
	v_pk_add_f32 v[100:101], v[94:95], 1.0 op_sel_hi:[1,0]
	v_pk_fma_f32 v[102:103], v[94:95], s[8:9], v[92:93] op_sel_hi:[1,0,0]
	v_pk_fma_f32 v[100:101], v[96:97], v[100:101], v[100:101]
	v_pk_fma_f32 v[104:105], v[100:101], v[98:99], v[100:101]
	v_rcp_f32_e32 v104, v104
	v_rcp_f32_e32 v105, v105
	v_pk_fma_f32 v[102:103], v[102:103], v[98:99], v[102:103]
	v_pk_fma_f32 v[102:103], v[64:65], v[100:101], v[102:103]
	v_exp_f32_e32 v106, v87
	v_pk_mul_f32 v[64:65], v[102:103], v[104:105]
	v_exp_f32_e32 v108, v64
	v_exp_f32_e32 v109, v65
	v_exp_f32_e32 v107, v91
	v_pk_add_f32 v[110:111], v[108:109], 1.0 op_sel_hi:[1,0]
	v_pk_fma_f32 v[110:111], v[110:111], v[106:107], v[110:111]
	v_rcp_f32_e32 v110, v110
	v_rcp_f32_e32 v111, v111
	v_pk_add_f32 v[112:113], v[108:109], -1.0 op_sel_hi:[1,0]
	v_pk_mul_f32 v[112:113], v[112:113], v[110:111]
	v_cvt_pk_f16_f32 v114, v112, v113
	ds_write_b32 v81, v114 offset:4096
	s_waitcnt lgkmcnt(1)
	v_mfma_f32_16x16x32_f16 v[84:87], v[2:5], v[44:47], v[18:21]
	v_mfma_f32_16x16x32_f16 v[88:91], v[14:17], v[44:47], v[38:41]
	v_mfma_f32_16x16x32_f16 v[84:87], v[6:9], v[68:71], v[84:87]
	v_mfma_f32_16x16x32_f16 v[88:91], v[10:13], v[68:71], v[88:91]
	s_waitcnt lgkmcnt(0)
	s_barrier
	ds_read_b128 v[56:59], v75 offset:4096
	ds_read_b128 v[60:63], v75 offset:5120
	ds_read_b128 v[44:47], v75 offset:0
	ds_read_b128 v[68:71], v75 offset:1024
	s_waitcnt lgkmcnt(3)
	v_mfma_f32_16x16x32_f16 v[84:87], v[30:33], v[56:59], v[84:87]
	v_mfma_f32_16x16x32_f16 v[88:91], v[22:25], v[56:59], v[88:91]
	s_waitcnt lgkmcnt(2)
	v_mfma_f32_16x16x32_f16 v[84:87], v[34:37], v[60:63], v[84:87]
	v_mfma_f32_16x16x32_f16 v[88:91], v[26:29], v[60:63], v[88:91]
	v_mfma_f32_16x16x32_f16 v[50:53], v[120:123], v[60:63], 0
	s_nop 7
	v_exp_f32_e32 v94, v86
	v_exp_f32_e32 v95, v90
	v_exp_f32_e32 v96, v84
	v_exp_f32_e32 v97, v88
	v_exp_f32_e32 v98, v85
	v_exp_f32_e32 v99, v89
	v_add_f32_e32 v125, v50, v51
	s_mov_b64 s[16:17], exec
	s_mov_b64 exec, s[30:31]
	ds_write_b32 v74, v125 offset:192
	s_mov_b64 exec, s[16:17]
	v_pk_add_f32 v[100:101], v[94:95], 1.0 op_sel_hi:[1,0]
	v_pk_fma_f32 v[102:103], v[94:95], s[8:9], v[92:93] op_sel_hi:[1,0,0]
	v_pk_fma_f32 v[100:101], v[96:97], v[100:101], v[100:101]
	v_pk_fma_f32 v[104:105], v[100:101], v[98:99], v[100:101]
	v_rcp_f32_e32 v104, v104
	v_rcp_f32_e32 v105, v105
	v_pk_fma_f32 v[102:103], v[102:103], v[98:99], v[102:103]
	v_pk_fma_f32 v[102:103], v[64:65], v[100:101], v[102:103]
	v_exp_f32_e32 v106, v87
	v_pk_mul_f32 v[64:65], v[102:103], v[104:105]
	v_exp_f32_e32 v108, v64
	v_exp_f32_e32 v109, v65
	v_exp_f32_e32 v107, v91
	v_pk_add_f32 v[110:111], v[108:109], 1.0 op_sel_hi:[1,0]
	v_pk_fma_f32 v[110:111], v[110:111], v[106:107], v[110:111]
	v_rcp_f32_e32 v110, v110
	v_rcp_f32_e32 v111, v111
	v_pk_add_f32 v[112:113], v[108:109], -1.0 op_sel_hi:[1,0]
	v_pk_mul_f32 v[112:113], v[112:113], v[110:111]
	v_cvt_pk_f16_f32 v114, v112, v113
	ds_write_b32 v81, v114 offset:6144
	s_waitcnt lgkmcnt(1)
	v_mfma_f32_16x16x32_f16 v[84:87], v[2:5], v[44:47], v[18:21]
	v_mfma_f32_16x16x32_f16 v[88:91], v[14:17], v[44:47], v[38:41]
	v_mfma_f32_16x16x32_f16 v[84:87], v[6:9], v[68:71], v[84:87]
	v_mfma_f32_16x16x32_f16 v[88:91], v[10:13], v[68:71], v[88:91]
	s_waitcnt lgkmcnt(0)
	v_min_f32_e32 v64, 0x42700000, v64
	v_min_f32_e32 v65, 0x42700000, v65
	s_add_u32 s12, s12, 4
	v_add_u32_e32 v124, 16, v124
	s_cmp_lt_u32 s12, 452
	s_cbranch_scc1 .Lcb1_loop
	s_barrier
	ds_read_b128 v[56:59], v75 offset:6144
	ds_read_b128 v[60:63], v75 offset:7168
	s_waitcnt lgkmcnt(0)
	v_mfma_f32_16x16x32_f16 v[50:53], v[120:123], v[60:63], 0
	s_nop 7
	v_add_f32_e32 v125, v50, v51
	s_mov_b64 s[16:17], exec
	s_mov_b64 exec, s[30:31]
	ds_write_b32 v74, v125 offset:64
	s_mov_b64 exec, s[16:17]
	s_waitcnt lgkmcnt(0)
	s_barrier
	s_waitcnt lgkmcnt(0)
	s_endpgm
.Lcb_r2:
	s_barrier
	ds_read_b128 v[44:47], v75 offset:0
	ds_read_b128 v[68:71], v75 offset:1024
	s_waitcnt lgkmcnt(0)
	v_mfma_f32_16x16x32_f16 v[84:87], v[2:5], v[44:47], v[18:21]
	v_mfma_f32_16x16x32_f16 v[88:91], v[14:17], v[44:47], v[38:41]
	v_mfma_f32_16x16x32_f16 v[84:87], v[6:9], v[68:71], v[84:87]
	v_mfma_f32_16x16x32_f16 v[88:91], v[10:13], v[68:71], v[88:91]
	s_barrier
	ds_read_b128 v[56:59], v75 offset:6144
	ds_read_b128 v[60:63], v75 offset:7168
	ds_read_b128 v[44:47], v75 offset:2048
	ds_read_b128 v[68:71], v75 offset:3072
	s_waitcnt lgkmcnt(3)
	v_mfma_f32_16x16x32_f16 v[84:87], v[30:33], v[56:59], v[84:87]
	v_mfma_f32_16x16x32_f16 v[88:91], v[22:25], v[56:59], v[88:91]
	s_waitcnt lgkmcnt(2)
	v_mfma_f32_16x16x32_f16 v[84:87], v[34:37], v[60:63], v[84:87]
	v_mfma_f32_16x16x32_f16 v[88:91], v[26:29], v[60:63], v[88:91]
	s_nop 7
	v_exp_f32_e32 v94, v86
	v_exp_f32_e32 v95, v90
	v_exp_f32_e32 v96, v84
	v_exp_f32_e32 v97, v88
	v_exp_f32_e32 v98, v85
	v_exp_f32_e32 v99, v89
	v_pk_add_f32 v[100:101], v[94:95], 1.0 op_sel_hi:[1,0]
	v_pk_fma_f32 v[102:103], v[94:95], s[8:9], v[92:93] op_sel_hi:[1,0,0]
	v_pk_fma_f32 v[100:101], v[96:97], v[100:101], v[100:101]
	v_pk_fma_f32 v[104:105], v[100:101], v[98:99], v[100:101]
	v_rcp_f32_e32 v104, v104
	v_rcp_f32_e32 v105, v105
	v_pk_fma_f32 v[102:103], v[102:103], v[98:99], v[102:103]
	v_pk_fma_f32 v[102:103], v[64:65], v[100:101], v[102:103]
	v_exp_f32_e32 v106, v87
	v_pk_mul_f32 v[64:65], v[102:103], v[104:105]
	v_exp_f32_e32 v108, v64
	v_exp_f32_e32 v109, v65
	v_exp_f32_e32 v107, v91
	v_pk_add_f32 v[110:111], v[108:109], 1.0 op_sel_hi:[1,0]
	v_pk_fma_f32 v[110:111], v[110:111], v[106:107], v[110:111]
	v_rcp_f32_e32 v110, v110
	v_rcp_f32_e32 v111, v111
	v_pk_add_f32 v[112:113], v[108:109], -1.0 op_sel_hi:[1,0]
	v_pk_mul_f32 v[112:113], v[112:113], v[110:111]
	v_cvt_pk_f16_f32 v114, v112, v113
	ds_write_b32 v81, v114 offset:4096
	s_waitcnt lgkmcnt(1)
	v_mfma_f32_16x16x32_f16 v[84:87], v[2:5], v[44:47], v[18:21]
	v_mfma_f32_16x16x32_f16 v[88:91], v[14:17], v[44:47], v[38:41]
	v_mfma_f32_16x16x32_f16 v[84:87], v[6:9], v[68:71], v[84:87]
	v_mfma_f32_16x16x32_f16 v[88:91], v[10:13], v[68:71], v[88:91]
	s_waitcnt lgkmcnt(0)
	s_barrier
	ds_read_b128 v[56:59], v75 offset:4096
	ds_read_b128 v[60:63], v75 offset:5120
	ds_read_b128 v[44:47], v75 offset:0
	ds_read_b128 v[68:71], v75 offset:1024
	s_waitcnt lgkmcnt(3)
	v_mfma_f32_16x16x32_f16 v[84:87], v[30:33], v[56:59], v[84:87]
	v_mfma_f32_16x16x32_f16 v[88:91], v[22:25], v[56:59], v[88:91]
	s_waitcnt lgkmcnt(2)
	v_mfma_f32_16x16x32_f16 v[84:87], v[34:37], v[60:63], v[84:87]
	v_mfma_f32_16x16x32_f16 v[88:91], v[26:29], v[60:63], v[88:91]
	s_nop 7
	v_exp_f32_e32 v94, v86
	v_exp_f32_e32 v95, v90
	v_exp_f32_e32 v96, v84
	v_exp_f32_e32 v97, v88
	v_exp_f32_e32 v98, v85
	v_exp_f32_e32 v99, v89
	v_pk_add_f32 v[100:101], v[94:95], 1.0 op_sel_hi:[1,0]
	v_pk_fma_f32 v[102:103], v[94:95], s[8:9], v[92:93] op_sel_hi:[1,0,0]
	v_pk_fma_f32 v[100:101], v[96:97], v[100:101], v[100:101]
	v_pk_fma_f32 v[104:105], v[100:101], v[98:99], v[100:101]
	v_rcp_f32_e32 v104, v104
	v_rcp_f32_e32 v105, v105
	v_pk_fma_f32 v[102:103], v[102:103], v[98:99], v[102:103]
	v_pk_fma_f32 v[102:103], v[64:65], v[100:101], v[102:103]
	v_exp_f32_e32 v106, v87
	v_pk_mul_f32 v[64:65], v[102:103], v[104:105]
	v_exp_f32_e32 v108, v64
	v_exp_f32_e32 v109, v65
	v_exp_f32_e32 v107, v91
	v_pk_add_f32 v[110:111], v[108:109], 1.0 op_sel_hi:[1,0]
	v_pk_fma_f32 v[110:111], v[110:111], v[106:107], v[110:111]
	v_rcp_f32_e32 v110, v110
	v_rcp_f32_e32 v111, v111
	v_pk_add_f32 v[112:113], v[108:109], -1.0 op_sel_hi:[1,0]
	v_pk_mul_f32 v[112:113], v[112:113], v[110:111]
	v_cvt_pk_f16_f32 v114, v112, v113
	ds_write_b32 v81, v114 offset:6144
	s_waitcnt lgkmcnt(1)
	v_mfma_f32_16x16x32_f16 v[84:87], v[2:5], v[44:47], v[18:21]
	v_mfma_f32_16x16x32_f16 v[88:91], v[14:17], v[44:47], v[38:41]
	v_mfma_f32_16x16x32_f16 v[84:87], v[6:9], v[68:71], v[84:87]
	v_mfma_f32_16x16x32_f16 v[88:91], v[10:13], v[68:71], v[88:91]
	s_waitcnt lgkmcnt(0)
	.p2align	6
.Lcb2_loop:
	s_barrier
	ds_read_b32 v125, v74 offset:128
	ds_read_b32 v126, v74 offset:192
	ds_read_b128 v[56:59], v75 offset:6144
	ds_read_b128 v[60:63], v75 offset:7168
	ds_read_b128 v[44:47], v75 offset:2048
	ds_read_b128 v[68:71], v75 offset:3072
	s_waitcnt lgkmcnt(4)
	v_add_f32_e32 v125, v125, v126
	v_mul_f32_e32 v126, 0x3fb8aa3b, v125
	v_exp_f32_e32 v126, v126
	v_cmp_lt_f32_e32 vcc, 0, v125
	v_mul_f32_e32 v125, 0x3f867d5f, v125
	v_fma_f32 v126, v126, v72, v73
	s_nop 0
	v_cndmask_b32_e32 v125, v126, v125, vcc
	s_mov_b64 s[16:17], exec
	s_mov_b64 exec, s[30:31]
	global_store_dword v124, v125, s[26:27] offset:0
	s_mov_b64 exec, s[16:17]
	s_waitcnt lgkmcnt(3)
	v_mfma_f32_16x16x32_f16 v[84:87], v[30:33], v[56:59], v[84:87]
	v_mfma_f32_16x16x32_f16 v[88:91], v[22:25], v[56:59], v[88:91]
	s_waitcnt lgkmcnt(2)
	v_mfma_f32_16x16x32_f16 v[84:87], v[34:37], v[60:63], v[84:87]
	v_mfma_f32_16x16x32_f16 v[88:91], v[26:29], v[60:63], v[88:91]
	s_nop 7
	v_exp_f32_e32 v94, v86
	v_exp_f32_e32 v95, v90
	v_exp_f32_e32 v96, v84
	v_exp_f32_e32 v97, v88
	v_exp_f32_e32 v98, v85
	v_exp_f32_e32 v99, v89
	v_pk_add_f32 v[100:101], v[94:95], 1.0 op_sel_hi:[1,0]
	v_pk_fma_f32 v[102:103], v[94:95], s[8:9], v[92:93] op_sel_hi:[1,0,0]
	v_pk_fma_f32 v[100:101], v[96:97], v[100:101], v[100:101]
	v_pk_fma_f32 v[104:105], v[100:101], v[98:99], v[100:101]
	v_rcp_f32_e32 v104, v104
	v_rcp_f32_e32 v105, v105
	v_pk_fma_f32 v[102:103], v[102:103], v[98:99], v[102:103]
	v_pk_fma_f32 v[102:103], v[64:65], v[100:101], v[102:103]
	v_exp_f32_e32 v106, v87
	v_pk_mul_f32 v[64:65], v[102:103], v[104:105]
	v_exp_f32_e32 v108, v64
	v_exp_f32_e32 v109, v65
	v_exp_f32_e32 v107, v91
	v_pk_add_f32 v[110:111], v[108:109], 1.0 op_sel_hi:[1,0]
	v_pk_fma_f32 v[110:111], v[110:111], v[106:107], v[110:111]
	v_rcp_f32_e32 v110, v110
	v_rcp_f32_e32 v111, v111
	v_pk_add_f32 v[112:113], v[108:109], -1.0 op_sel_hi:[1,0]
	v_pk_mul_f32 v[112:113], v[112:113], v[110:111]
	v_cvt_pk_f16_f32 v114, v112, v113
	ds_write_b32 v81, v114 offset:4096
	s_waitcnt lgkmcnt(1)
	v_mfma_f32_16x16x32_f16 v[84:87], v[2:5], v[44:47], v[18:21]
	v_mfma_f32_16x16x32_f16 v[88:91], v[14:17], v[44:47], v[38:41]
	v_mfma_f32_16x16x32_f16 v[84:87], v[6:9], v[68:71], v[84:87]
	v_mfma_f32_16x16x32_f16 v[88:91], v[10:13], v[68:71], v[88:91]
	s_waitcnt lgkmcnt(0)
	s_barrier
	ds_read_b32 v125, v74 offset:0
	ds_read_b32 v126, v74 offset:64
	ds_read_b128 v[56:59], v75 offset:4096
	ds_read_b128 v[60:63], v75 offset:5120
	ds_read_b128 v[44:47], v75 offset:0
	ds_read_b128 v[68:71], v75 offset:1024
	s_waitcnt lgkmcnt(4)
	v_add_f32_e32 v125, v125, v126
	v_mul_f32_e32 v126, 0x3fb8aa3b, v125
	v_exp_f32_e32 v126, v126
	v_cmp_lt_f32_e32 vcc, 0, v125
	v_mul_f32_e32 v125, 0x3f867d5f, v125
	v_fma_f32 v126, v126, v72, v73
	s_nop 0
	v_cndmask_b32_e32 v125, v126, v125, vcc
	s_mov_b64 s[16:17], exec
	s_mov_b64 exec, s[30:31]
	global_store_dword v124, v125, s[26:27] offset:4
	s_mov_b64 exec, s[16:17]
	s_waitcnt lgkmcnt(3)
	v_mfma_f32_16x16x32_f16 v[84:87], v[30:33], v[56:59], v[84:87]
	v_mfma_f32_16x16x32_f16 v[88:91], v[22:25], v[56:59], v[88:91]
	s_waitcnt lgkmcnt(2)
	v_mfma_f32_16x16x32_f16 v[84:87], v[34:37], v[60:63], v[84:87]
	v_mfma_f32_16x16x32_f16 v[88:91], v[26:29], v[60:63], v[88:91]
	s_nop 7
	v_exp_f32_e32 v94, v86
	v_exp_f32_e32 v95, v90
	v_exp_f32_e32 v96, v84
	v_exp_f32_e32 v97, v88
	v_exp_f32_e32 v98, v85
	v_exp_f32_e32 v99, v89
	v_pk_add_f32 v[100:101], v[94:95], 1.0 op_sel_hi:[1,0]
	v_pk_fma_f32 v[102:103], v[94:95], s[8:9], v[92:93] op_sel_hi:[1,0,0]
	v_pk_fma_f32 v[100:101], v[96:97], v[100:101], v[100:101]
	v_pk_fma_f32 v[104:105], v[100:101], v[98:99], v[100:101]
	v_rcp_f32_e32 v104, v104
	v_rcp_f32_e32 v105, v105
	v_pk_fma_f32 v[102:103], v[102:103], v[98:99], v[102:103]
	v_pk_fma_f32 v[102:103], v[64:65], v[100:101], v[102:103]
	v_exp_f32_e32 v106, v87
	v_pk_mul_f32 v[64:65], v[102:103], v[104:105]
	v_exp_f32_e32 v108, v64
	v_exp_f32_e32 v109, v65
	v_exp_f32_e32 v107, v91
	v_pk_add_f32 v[110:111], v[108:109], 1.0 op_sel_hi:[1,0]
	v_pk_fma_f32 v[110:111], v[110:111], v[106:107], v[110:111]
	v_rcp_f32_e32 v110, v110
	v_rcp_f32_e32 v111, v111
	v_pk_add_f32 v[112:113], v[108:109], -1.0 op_sel_hi:[1,0]
	v_pk_mul_f32 v[112:113], v[112:113], v[110:111]
	v_cvt_pk_f16_f32 v114, v112, v113
	ds_write_b32 v81, v114 offset:6144
	s_waitcnt lgkmcnt(1)
	v_mfma_f32_16x16x32_f16 v[84:87], v[2:5], v[44:47], v[18:21]
	v_mfma_f32_16x16x32_f16 v[88:91], v[14:17], v[44:47], v[38:41]
	v_mfma_f32_16x16x32_f16 v[84:87], v[6:9], v[68:71], v[84:87]
	v_mfma_f32_16x16x32_f16 v[88:91], v[10:13], v[68:71], v[88:91]
	s_waitcnt lgkmcnt(0)
	s_barrier
	ds_read_b32 v125, v74 offset:128
	ds_read_b32 v126, v74 offset:192
	ds_read_b128 v[56:59], v75 offset:6144
	ds_read_b128 v[60:63], v75 offset:7168
	ds_read_b128 v[44:47], v75 offset:2048
	ds_read_b128 v[68:71], v75 offset:3072
	s_waitcnt lgkmcnt(4)
	v_add_f32_e32 v125, v125, v126
	v_mul_f32_e32 v126, 0x3fb8aa3b, v125
	v_exp_f32_e32 v126, v126
	v_cmp_lt_f32_e32 vcc, 0, v125
	v_mul_f32_e32 v125, 0x3f867d5f, v125
	v_fma_f32 v126, v126, v72, v73
	s_nop 0
	v_cndmask_b32_e32 v125, v126, v125, vcc
	s_mov_b64 s[16:17], exec
	s_mov_b64 exec, s[30:31]
	global_store_dword v124, v125, s[26:27] offset:8
	s_mov_b64 exec, s[16:17]
	s_waitcnt lgkmcnt(3)
	v_mfma_f32_16x16x32_f16 v[84:87], v[30:33], v[56:59], v[84:87]
	v_mfma_f32_16x16x32_f16 v[88:91], v[22:25], v[56:59], v[88:91]
	s_waitcnt lgkmcnt(2)
	v_mfma_f32_16x16x32_f16 v[84:87], v[34:37], v[60:63], v[84:87]
	v_mfma_f32_16x16x32_f16 v[88:91], v[26:29], v[60:63], v[88:91]
	s_nop 7
	v_exp_f32_e32 v94, v86
	v_exp_f32_e32 v95, v90
	v_exp_f32_e32 v96, v84
	v_exp_f32_e32 v97, v88
	v_exp_f32_e32 v98, v85
	v_exp_f32_e32 v99, v89
	v_pk_add_f32 v[100:101], v[94:95], 1.0 op_sel_hi:[1,0]
	v_pk_fma_f32 v[102:103], v[94:95], s[8:9], v[92:93] op_sel_hi:[1,0,0]
	v_pk_fma_f32 v[100:101], v[96:97], v[100:101], v[100:101]
	v_pk_fma_f32 v[104:105], v[100:101], v[98:99], v[100:101]
	v_rcp_f32_e32 v104, v104
	v_rcp_f32_e32 v105, v105
	v_pk_fma_f32 v[102:103], v[102:103], v[98:99], v[102:103]
	v_pk_fma_f32 v[102:103], v[64:65], v[100:101], v[102:103]
	v_exp_f32_e32 v106, v87
	v_pk_mul_f32 v[64:65], v[102:103], v[104:105]
	v_exp_f32_e32 v108, v64
	v_exp_f32_e32 v109, v65
	v_exp_f32_e32 v107, v91
	v_pk_add_f32 v[110:111], v[108:109], 1.0 op_sel_hi:[1,0]
	v_pk_fma_f32 v[110:111], v[110:111], v[106:107], v[110:111]
	v_rcp_f32_e32 v110, v110
	v_rcp_f32_e32 v111, v111
	v_pk_add_f32 v[112:113], v[108:109], -1.0 op_sel_hi:[1,0]
	v_pk_mul_f32 v[112:113], v[112:113], v[110:111]
	v_cvt_pk_f16_f32 v114, v112, v113
	ds_write_b32 v81, v114 offset:4096
	s_waitcnt lgkmcnt(1)
	v_mfma_f32_16x16x32_f16 v[84:87], v[2:5], v[44:47], v[18:21]
	v_mfma_f32_16x16x32_f16 v[88:91], v[14:17], v[44:47], v[38:41]
	v_mfma_f32_16x16x32_f16 v[84:87], v[6:9], v[68:71], v[84:87]
	v_mfma_f32_16x16x32_f16 v[88:91], v[10:13], v[68:71], v[88:91]
	s_waitcnt lgkmcnt(0)
	s_barrier
	ds_read_b32 v125, v74 offset:0
	ds_read_b32 v126, v74 offset:64
	ds_read_b128 v[56:59], v75 offset:4096
	ds_read_b128 v[60:63], v75 offset:5120
	ds_read_b128 v[44:47], v75 offset:0
	ds_read_b128 v[68:71], v75 offset:1024
	s_waitcnt lgkmcnt(4)
	v_add_f32_e32 v125, v125, v126
	v_mul_f32_e32 v126, 0x3fb8aa3b, v125
	v_exp_f32_e32 v126, v126
	v_cmp_lt_f32_e32 vcc, 0, v125
	v_mul_f32_e32 v125, 0x3f867d5f, v125
	v_fma_f32 v126, v126, v72, v73
	s_nop 0
	v_cndmask_b32_e32 v125, v126, v125, vcc
	s_mov_b64 s[16:17], exec
	s_mov_b64 exec, s[30:31]
	global_store_dword v124, v125, s[26:27] offset:12
	s_mov_b64 exec, s[16:17]
	s_waitcnt lgkmcnt(3)
	v_mfma_f32_16x16x32_f16 v[84:87], v[30:33], v[56:59], v[84:87]
	v_mfma_f32_16x16x32_f16 v[88:91], v[22:25], v[56:59], v[88:91]
	s_waitcnt lgkmcnt(2)
	v_mfma_f32_16x16x32_f16 v[84:87], v[34:37], v[60:63], v[84:87]
	v_mfma_f32_16x16x32_f16 v[88:91], v[26:29], v[60:63], v[88:91]
	s_nop 7
	v_exp_f32_e32 v94, v86
	v_exp_f32_e32 v95, v90
	v_exp_f32_e32 v96, v84
	v_exp_f32_e32 v97, v88
	v_exp_f32_e32 v98, v85
	v_exp_f32_e32 v99, v89
	v_pk_add_f32 v[100:101], v[94:95], 1.0 op_sel_hi:[1,0]
	v_pk_fma_f32 v[102:103], v[94:95], s[8:9], v[92:93] op_sel_hi:[1,0,0]
	v_pk_fma_f32 v[100:101], v[96:97], v[100:101], v[100:101]
	v_pk_fma_f32 v[104:105], v[100:101], v[98:99], v[100:101]
	v_rcp_f32_e32 v104, v104
	v_rcp_f32_e32 v105, v105
	v_pk_fma_f32 v[102:103], v[102:103], v[98:99], v[102:103]
	v_pk_fma_f32 v[102:103], v[64:65], v[100:101], v[102:103]
	v_exp_f32_e32 v106, v87
	v_pk_mul_f32 v[64:65], v[102:103], v[104:105]
	v_exp_f32_e32 v108, v64
	v_exp_f32_e32 v109, v65
	v_exp_f32_e32 v107, v91
	v_pk_add_f32 v[110:111], v[108:109], 1.0 op_sel_hi:[1,0]
	v_pk_fma_f32 v[110:111], v[110:111], v[106:107], v[110:111]
	v_rcp_f32_e32 v110, v110
	v_rcp_f32_e32 v111, v111
	v_pk_add_f32 v[112:113], v[108:109], -1.0 op_sel_hi:[1,0]
	v_pk_mul_f32 v[112:113], v[112:113], v[110:111]
	v_cvt_pk_f16_f32 v114, v112, v113
	ds_write_b32 v81, v114 offset:6144
	s_waitcnt lgkmcnt(1)
	v_mfma_f32_16x16x32_f16 v[84:87], v[2:5], v[44:47], v[18:21]
	v_mfma_f32_16x16x32_f16 v[88:91], v[14:17], v[44:47], v[38:41]
	v_mfma_f32_16x16x32_f16 v[84:87], v[6:9], v[68:71], v[84:87]
	v_mfma_f32_16x16x32_f16 v[88:91], v[10:13], v[68:71], v[88:91]
	s_waitcnt lgkmcnt(0)
	v_min_f32_e32 v64, 0x42700000, v64
	v_min_f32_e32 v65, 0x42700000, v65
	s_add_u32 s12, s12, 4
	v_add_u32_e32 v124, 16, v124
	s_cmp_lt_u32 s12, 452
	s_cbranch_scc1 .Lcb2_loop
	s_barrier
	ds_read_b32 v125, v74 offset:128
	ds_read_b32 v126, v74 offset:192
	ds_read_b128 v[56:59], v75 offset:6144
	ds_read_b128 v[60:63], v75 offset:7168
	s_waitcnt lgkmcnt(2)
	v_add_f32_e32 v125, v125, v126
	v_mul_f32_e32 v126, 0x3fb8aa3b, v125
	v_exp_f32_e32 v126, v126
	v_cmp_lt_f32_e32 vcc, 0, v125
	v_mul_f32_e32 v125, 0x3f867d5f, v125
	v_fma_f32 v126, v126, v72, v73
	s_nop 0
	v_cndmask_b32_e32 v125, v126, v125, vcc
	s_mov_b64 s[16:17], exec
	s_mov_b64 exec, s[30:31]
	global_store_dword v124, v125, s[26:27] offset:0
	s_mov_b64 exec, s[16:17]
	s_waitcnt lgkmcnt(0)
	s_waitcnt lgkmcnt(0)
	s_barrier
	ds_read_b32 v125, v74 offset:0
	ds_read_b32 v126, v74 offset:64
	s_waitcnt lgkmcnt(0)
	v_add_f32_e32 v125, v125, v126
	v_mul_f32_e32 v126, 0x3fb8aa3b, v125
	v_exp_f32_e32 v126, v126
	v_cmp_lt_f32_e32 vcc, 0, v125
	v_mul_f32_e32 v125, 0x3f867d5f, v125
	v_fma_f32 v126, v126, v72, v73
	s_nop 0
	v_cndmask_b32_e32 v125, v126, v125, vcc
	s_mov_b64 s[16:17], exec
	s_mov_b64 exec, s[30:31]
	global_store_dword v124, v125, s[26:27] offset:4
	s_mov_b64 exec, s[16:17]
	s_waitcnt lgkmcnt(0)
	s_endpgm

.Lk_144:
	v_or_b32_e32 v46, 0x400, v54
	buffer_load_dwordx4 v[46:49], v46, s[4:7], 0 offen sc1
	ds_read_b128 v[50:53], v1
	v_mov_b32_e32 v66, 0
	v_add_u32_e32 v63, 0x800, v54
	s_mov_b32 s9, 0
	v_mov_b32_e32 v67, 0
	v_mov_b32_e32 v68, 0
	v_mov_b32_e32 v62, 0xc038aa3b
	s_mov_b32 s8, 0x4038aa3b
	v_mov_b32_e32 v65, 0
	v_mov_b32_e32 v64, v66
	s_setprio 2
	v_mov_b32_e32 v92, 0xc038aa3b
	v_mov_b32_e32 v93, 0xc038aa3b
	s_mov_b32 s8, 0x4038aa3b
	s_mov_b32 s9, 0
	v_mov_b32_e32 v64, 0
	v_mov_b32_e32 v65, 0
	v_mov_b32_e32 v66, 0
	v_mov_b32_e32 v67, 0
	v_mov_b32_e32 v68, 0
	v_mov_b32_e32 v116, v1
	v_mov_b32_e32 v117, v63
	s_mov_b32 s12, 0
	s_waitcnt lgkmcnt(0)
	v_mfma_f32_16x16x32_f16 v[84:87], v[6:9], v[50:53], v[18:21]
	v_mfma_f32_16x16x32_f16 v[88:91], v[10:13], v[50:53], v[38:41]
	ds_read_b128 v[56:59], v75 offset:2048
	ds_read_b128 v[60:63], v75 offset:3072
	s_waitcnt vmcnt(1)
	v_mfma_f32_16x16x32_f16 v[84:87], v[2:5], v[42:45], v[84:87]
	v_mfma_f32_16x16x32_f16 v[88:91], v[14:17], v[42:45], v[88:91]
	v_readfirstlane_b32 s10, v67
	v_readfirstlane_b32 s11, v68
	global_load_dword v67, v66, s[0:1] sc1
	global_load_dword v68, v66, s[0:1] offset:4 sc1
	s_min_u32 s10, s10, s11
	s_max_u32 s14, s14, s10
	s_waitcnt lgkmcnt(1)
	v_mfma_f32_16x16x32_f16 v[84:87], v[30:33], v[56:59], v[84:87]
	v_mfma_f32_16x16x32_f16 v[88:91], v[22:25], v[56:59], v[88:91]
	s_waitcnt lgkmcnt(0)
	v_mfma_f32_16x16x32_f16 v[84:87], v[34:37], v[60:63], v[84:87]
	v_mfma_f32_16x16x32_f16 v[88:91], v[26:29], v[60:63], v[88:91]
	s_add_u32 s13, s12, 3
	s_min_u32 s13, s13, 450
	s_cmp_ge_u32 s14, s13
	s_cbranch_scc0 .Lca_slow_3
.Lca_ok_1:
	buffer_load_dwordx4 v[42:45], v117, s[4:7], 0 offen offset:0 sc1
	ds_read_b128 v[50:53], v116 offset:256
	s_nop 1
	v_exp_f32_e32 v94, v86
	v_exp_f32_e32 v95, v90
	v_exp_f32_e32 v96, v84
	v_exp_f32_e32 v97, v88
	v_exp_f32_e32 v98, v85
	v_exp_f32_e32 v99, v89
	v_pk_add_f32 v[100:101], v[94:95], 1.0 op_sel_hi:[1,0]
	v_pk_fma_f32 v[102:103], v[94:95], s[8:9], v[92:93] op_sel_hi:[1,0,0]
	v_pk_fma_f32 v[100:101], v[96:97], v[100:101], v[100:101]
	v_pk_fma_f32 v[104:105], v[100:101], v[98:99], v[100:101]
	v_rcp_f32_e32 v104, v104
	v_rcp_f32_e32 v105, v105
	v_pk_fma_f32 v[102:103], v[102:103], v[98:99], v[102:103]
	v_pk_fma_f32 v[102:103], v[64:65], v[100:101], v[102:103]
	v_exp_f32_e32 v106, v87
	v_pk_mul_f32 v[64:65], v[102:103], v[104:105]
	v_exp_f32_e32 v108, v64
	v_exp_f32_e32 v109, v65
	v_exp_f32_e32 v107, v91
	v_pk_add_f32 v[110:111], v[108:109], 1.0 op_sel_hi:[1,0]
	v_pk_fma_f32 v[110:111], v[110:111], v[106:107], v[110:111]
	v_rcp_f32_e32 v110, v110
	v_rcp_f32_e32 v111, v111
	v_pk_add_f32 v[112:113], v[108:109], -1.0 op_sel_hi:[1,0]
	v_pk_mul_f32 v[112:113], v[112:113], v[110:111]
	v_cvt_pk_f16_f32 v114, v112, v113
	ds_write_b32 v81, v114 offset:0
	s_waitcnt lgkmcnt(0)
	s_barrier
	v_mfma_f32_16x16x32_f16 v[84:87], v[6:9], v[50:53], v[18:21]
	v_mfma_f32_16x16x32_f16 v[88:91], v[10:13], v[50:53], v[38:41]
	ds_read_b128 v[56:59], v75 offset:0
	ds_read_b128 v[60:63], v75 offset:1024
	s_waitcnt vmcnt(3)
	v_mfma_f32_16x16x32_f16 v[84:87], v[2:5], v[46:49], v[84:87]
	v_mfma_f32_16x16x32_f16 v[88:91], v[14:17], v[46:49], v[88:91]
	s_waitcnt lgkmcnt(1)
	v_mfma_f32_16x16x32_f16 v[84:87], v[30:33], v[56:59], v[84:87]
	v_mfma_f32_16x16x32_f16 v[88:91], v[22:25], v[56:59], v[88:91]
	s_waitcnt lgkmcnt(0)
	v_mfma_f32_16x16x32_f16 v[84:87], v[34:37], v[60:63], v[84:87]
	v_mfma_f32_16x16x32_f16 v[88:91], v[26:29], v[60:63], v[88:91]
	s_add_u32 s13, s12, 4
	s_min_u32 s13, s13, 450
	s_cmp_ge_u32 s14, s13
	s_cbranch_scc0 .Lca_slow_6
.Lca_ok_4:
	buffer_load_dwordx4 v[46:49], v117, s[4:7], 0 offen offset:1024 sc1
	ds_read_b128 v[50:53], v116 offset:512
	s_nop 1
	v_exp_f32_e32 v94, v86
	v_exp_f32_e32 v95, v90
	v_exp_f32_e32 v96, v84
	v_exp_f32_e32 v97, v88
	v_exp_f32_e32 v98, v85
	v_exp_f32_e32 v99, v89
	v_pk_add_f32 v[100:101], v[94:95], 1.0 op_sel_hi:[1,0]
	v_pk_fma_f32 v[102:103], v[94:95], s[8:9], v[92:93] op_sel_hi:[1,0,0]
	v_pk_fma_f32 v[100:101], v[96:97], v[100:101], v[100:101]
	v_pk_fma_f32 v[104:105], v[100:101], v[98:99], v[100:101]
	v_rcp_f32_e32 v104, v104
	v_rcp_f32_e32 v105, v105
	v_pk_fma_f32 v[102:103], v[102:103], v[98:99], v[102:103]
	v_pk_fma_f32 v[102:103], v[64:65], v[100:101], v[102:103]
	v_exp_f32_e32 v106, v87
	v_pk_mul_f32 v[64:65], v[102:103], v[104:105]
	v_exp_f32_e32 v108, v64
	v_exp_f32_e32 v109, v65
	v_exp_f32_e32 v107, v91
	v_pk_add_f32 v[110:111], v[108:109], 1.0 op_sel_hi:[1,0]
	v_pk_fma_f32 v[110:111], v[110:111], v[106:107], v[110:111]
	v_rcp_f32_e32 v110, v110
	v_rcp_f32_e32 v111, v111
	v_pk_add_f32 v[112:113], v[108:109], -1.0 op_sel_hi:[1,0]
	v_pk_mul_f32 v[112:113], v[112:113], v[110:111]
	v_cvt_pk_f16_f32 v114, v112, v113
	ds_write_b32 v81, v114 offset:2048
	s_waitcnt lgkmcnt(0)
	v_add_u32_e32 v116, 0x200, v116
	v_add_u32_e32 v117, 0x800, v117
	s_mov_b32 s12, 2
	.p2align	6
.Lca_loop:
	s_barrier
	v_mfma_f32_16x16x32_f16 v[84:87], v[6:9], v[50:53], v[18:21]
	v_mfma_f32_16x16x32_f16 v[88:91], v[10:13], v[50:53], v[38:41]
	ds_read_b128 v[56:59], v75 offset:2048
	ds_read_b128 v[60:63], v75 offset:3072
	s_waitcnt vmcnt(1)
	v_mfma_f32_16x16x32_f16 v[84:87], v[2:5], v[42:45], v[84:87]
	v_mfma_f32_16x16x32_f16 v[88:91], v[14:17], v[42:45], v[88:91]
	v_readfirstlane_b32 s10, v67
	v_readfirstlane_b32 s11, v68
	global_load_dword v67, v66, s[0:1] sc1
	global_load_dword v68, v66, s[0:1] offset:4 sc1
	s_min_u32 s10, s10, s11
	s_max_u32 s14, s14, s10
	s_waitcnt lgkmcnt(1)
	v_mfma_f32_16x16x32_f16 v[84:87], v[30:33], v[56:59], v[84:87]
	v_mfma_f32_16x16x32_f16 v[88:91], v[22:25], v[56:59], v[88:91]
	s_waitcnt lgkmcnt(0)
	v_mfma_f32_16x16x32_f16 v[84:87], v[34:37], v[60:63], v[84:87]
	v_mfma_f32_16x16x32_f16 v[88:91], v[26:29], v[60:63], v[88:91]
	s_add_u32 s13, s12, 3
	s_min_u32 s13, s13, 450
	s_cmp_ge_u32 s14, s13
	s_cbranch_scc0 .Lca_slow_9
.Lca_ok_7:
	buffer_load_dwordx4 v[42:45], v117, s[4:7], 0 offen offset:0 sc1
	ds_read_b128 v[50:53], v116 offset:256
	s_nop 1
	v_min_f32_e32 v64, 0x42700000, v64
	v_min_f32_e32 v65, 0x42700000, v65
	v_exp_f32_e32 v94, v86
	v_exp_f32_e32 v95, v90
	v_exp_f32_e32 v96, v84
	v_exp_f32_e32 v97, v88
	v_exp_f32_e32 v98, v85
	v_exp_f32_e32 v99, v89
	v_pk_add_f32 v[100:101], v[94:95], 1.0 op_sel_hi:[1,0]
	v_pk_fma_f32 v[102:103], v[94:95], s[8:9], v[92:93] op_sel_hi:[1,0,0]
	v_pk_fma_f32 v[100:101], v[96:97], v[100:101], v[100:101]
	v_pk_fma_f32 v[104:105], v[100:101], v[98:99], v[100:101]
	v_rcp_f32_e32 v104, v104
	v_rcp_f32_e32 v105, v105
	v_pk_fma_f32 v[102:103], v[102:103], v[98:99], v[102:103]
	v_pk_fma_f32 v[102:103], v[64:65], v[100:101], v[102:103]
	v_exp_f32_e32 v106, v87
	v_pk_mul_f32 v[64:65], v[102:103], v[104:105]
	v_exp_f32_e32 v108, v64
	v_exp_f32_e32 v109, v65
	v_exp_f32_e32 v107, v91
	v_pk_add_f32 v[110:111], v[108:109], 1.0 op_sel_hi:[1,0]
	v_pk_fma_f32 v[110:111], v[110:111], v[106:107], v[110:111]
	v_rcp_f32_e32 v110, v110
	v_rcp_f32_e32 v111, v111
	v_pk_add_f32 v[112:113], v[108:109], -1.0 op_sel_hi:[1,0]
	v_pk_mul_f32 v[112:113], v[112:113], v[110:111]
	v_cvt_pk_f16_f32 v114, v112, v113
	ds_write_b32 v81, v114 offset:0
	s_waitcnt lgkmcnt(0)
	s_barrier
	v_mfma_f32_16x16x32_f16 v[84:87], v[6:9], v[50:53], v[18:21]
	v_mfma_f32_16x16x32_f16 v[88:91], v[10:13], v[50:53], v[38:41]
	ds_read_b128 v[56:59], v75 offset:0
	ds_read_b128 v[60:63], v75 offset:1024
	s_waitcnt vmcnt(3)
	v_mfma_f32_16x16x32_f16 v[84:87], v[2:5], v[46:49], v[84:87]
	v_mfma_f32_16x16x32_f16 v[88:91], v[14:17], v[46:49], v[88:91]
	s_waitcnt lgkmcnt(1)
	v_mfma_f32_16x16x32_f16 v[84:87], v[30:33], v[56:59], v[84:87]
	v_mfma_f32_16x16x32_f16 v[88:91], v[22:25], v[56:59], v[88:91]
	s_waitcnt lgkmcnt(0)
	v_mfma_f32_16x16x32_f16 v[84:87], v[34:37], v[60:63], v[84:87]
	v_mfma_f32_16x16x32_f16 v[88:91], v[26:29], v[60:63], v[88:91]
	s_add_u32 s13, s12, 4
	s_min_u32 s13, s13, 450
	s_cmp_ge_u32 s14, s13
	s_cbranch_scc0 .Lca_slow_12
.Lca_ok_10:
	buffer_load_dwordx4 v[46:49], v117, s[4:7], 0 offen offset:1024 sc1
	ds_read_b128 v[50:53], v116 offset:512
	s_nop 1
	v_exp_f32_e32 v94, v86
	v_exp_f32_e32 v95, v90
	v_exp_f32_e32 v96, v84
	v_exp_f32_e32 v97, v88
	v_exp_f32_e32 v98, v85
	v_exp_f32_e32 v99, v89
	v_pk_add_f32 v[100:101], v[94:95], 1.0 op_sel_hi:[1,0]
	v_pk_fma_f32 v[102:103], v[94:95], s[8:9], v[92:93] op_sel_hi:[1,0,0]
	v_pk_fma_f32 v[100:101], v[96:97], v[100:101], v[100:101]
	v_pk_fma_f32 v[104:105], v[100:101], v[98:99], v[100:101]
	v_rcp_f32_e32 v104, v104
	v_rcp_f32_e32 v105, v105
	v_pk_fma_f32 v[102:103], v[102:103], v[98:99], v[102:103]
	v_pk_fma_f32 v[102:103], v[64:65], v[100:101], v[102:103]
	v_exp_f32_e32 v106, v87
	v_pk_mul_f32 v[64:65], v[102:103], v[104:105]
	v_exp_f32_e32 v108, v64
	v_exp_f32_e32 v109, v65
	v_exp_f32_e32 v107, v91
	v_pk_add_f32 v[110:111], v[108:109], 1.0 op_sel_hi:[1,0]
	v_pk_fma_f32 v[110:111], v[110:111], v[106:107], v[110:111]
	v_rcp_f32_e32 v110, v110
	v_rcp_f32_e32 v111, v111
	v_pk_add_f32 v[112:113], v[108:109], -1.0 op_sel_hi:[1,0]
	v_pk_mul_f32 v[112:113], v[112:113], v[110:111]
	v_cvt_pk_f16_f32 v114, v112, v113
	ds_write_b32 v81, v114 offset:2048
	s_waitcnt lgkmcnt(0)
	s_barrier
	v_mfma_f32_16x16x32_f16 v[84:87], v[6:9], v[50:53], v[18:21]
	v_mfma_f32_16x16x32_f16 v[88:91], v[10:13], v[50:53], v[38:41]
	ds_read_b128 v[56:59], v75 offset:2048
	ds_read_b128 v[60:63], v75 offset:3072
	s_waitcnt vmcnt(1)
	v_mfma_f32_16x16x32_f16 v[84:87], v[2:5], v[42:45], v[84:87]
	v_mfma_f32_16x16x32_f16 v[88:91], v[14:17], v[42:45], v[88:91]
	v_readfirstlane_b32 s10, v67
	v_readfirstlane_b32 s11, v68
	global_load_dword v67, v66, s[0:1] sc1
	global_load_dword v68, v66, s[0:1] offset:4 sc1
	s_min_u32 s10, s10, s11
	s_max_u32 s14, s14, s10
	s_waitcnt lgkmcnt(1)
	v_mfma_f32_16x16x32_f16 v[84:87], v[30:33], v[56:59], v[84:87]
	v_mfma_f32_16x16x32_f16 v[88:91], v[22:25], v[56:59], v[88:91]
	s_waitcnt lgkmcnt(0)
	v_mfma_f32_16x16x32_f16 v[84:87], v[34:37], v[60:63], v[84:87]
	v_mfma_f32_16x16x32_f16 v[88:91], v[26:29], v[60:63], v[88:91]
	s_add_u32 s13, s12, 5
	s_min_u32 s13, s13, 450
	s_cmp_ge_u32 s14, s13
	s_cbranch_scc0 .Lca_slow_15
.Lca_ok_13:
	buffer_load_dwordx4 v[42:45], v117, s[4:7], 0 offen offset:2048 sc1
	ds_read_b128 v[50:53], v116 offset:768
	s_nop 1
	v_exp_f32_e32 v94, v86
	v_exp_f32_e32 v95, v90
	v_exp_f32_e32 v96, v84
	v_exp_f32_e32 v97, v88
	v_exp_f32_e32 v98, v85
	v_exp_f32_e32 v99, v89
	v_pk_add_f32 v[100:101], v[94:95], 1.0 op_sel_hi:[1,0]
	v_pk_fma_f32 v[102:103], v[94:95], s[8:9], v[92:93] op_sel_hi:[1,0,0]
	v_pk_fma_f32 v[100:101], v[96:97], v[100:101], v[100:101]
	v_pk_fma_f32 v[104:105], v[100:101], v[98:99], v[100:101]
	v_rcp_f32_e32 v104, v104
	v_rcp_f32_e32 v105, v105
	v_pk_fma_f32 v[102:103], v[102:103], v[98:99], v[102:103]
	v_pk_fma_f32 v[102:103], v[64:65], v[100:101], v[102:103]
	v_exp_f32_e32 v106, v87
	v_pk_mul_f32 v[64:65], v[102:103], v[104:105]
	v_exp_f32_e32 v108, v64
	v_exp_f32_e32 v109, v65
	v_exp_f32_e32 v107, v91
	v_pk_add_f32 v[110:111], v[108:109], 1.0 op_sel_hi:[1,0]
	v_pk_fma_f32 v[110:111], v[110:111], v[106:107], v[110:111]
	v_rcp_f32_e32 v110, v110
	v_rcp_f32_e32 v111, v111
	v_pk_add_f32 v[112:113], v[108:109], -1.0 op_sel_hi:[1,0]
	v_pk_mul_f32 v[112:113], v[112:113], v[110:111]
	v_cvt_pk_f16_f32 v114, v112, v113
	ds_write_b32 v81, v114 offset:0
	s_waitcnt lgkmcnt(0)
	s_barrier
	v_mfma_f32_16x16x32_f16 v[84:87], v[6:9], v[50:53], v[18:21]
	v_mfma_f32_16x16x32_f16 v[88:91], v[10:13], v[50:53], v[38:41]
	ds_read_b128 v[56:59], v75 offset:0
	ds_read_b128 v[60:63], v75 offset:1024
	s_waitcnt vmcnt(3)
	v_mfma_f32_16x16x32_f16 v[84:87], v[2:5], v[46:49], v[84:87]
	v_mfma_f32_16x16x32_f16 v[88:91], v[14:17], v[46:49], v[88:91]
	s_waitcnt lgkmcnt(1)
	v_mfma_f32_16x16x32_f16 v[84:87], v[30:33], v[56:59], v[84:87]
	v_mfma_f32_16x16x32_f16 v[88:91], v[22:25], v[56:59], v[88:91]
	s_waitcnt lgkmcnt(0)
	v_mfma_f32_16x16x32_f16 v[84:87], v[34:37], v[60:63], v[84:87]
	v_mfma_f32_16x16x32_f16 v[88:91], v[26:29], v[60:63], v[88:91]
	s_add_u32 s13, s12, 6
	s_min_u32 s13, s13, 450
	s_cmp_ge_u32 s14, s13
	s_cbranch_scc0 .Lca_slow_18

.Lca_slow_3:
	s_mov_b32 s15, 0

.Lca_spin_17:
	global_load_dword v67, v66, s[0:1] sc1
	global_load_dword v68, v66, s[0:1] offset:4 sc1
	s_waitcnt vmcnt(0)
	v_readfirstlane_b32 s10, v67
	v_readfirstlane_b32 s11, v68
	s_nop 1
	s_min_u32 s10, s10, s11
	s_max_u32 s14, s14, s10
	s_cmp_ge_u32 s14, s13
	s_cbranch_scc1 .Lca_ok_16
	s_add_u32 s15, s15, 1
	s_cmp_lt_u32 s15, 0x400000
	s_cbranch_scc0 .Lca_ok_16
	s_sleep 4
	s_branch .Lca_spin_17
.Lk_216:
	s_mov_b64 s[0:1], 0

.Lk_220:
	v_or_b32_e32 v18, 0x400, v0
	v_add_u32_e32 v1, s33, v18
	v_add_u32_e32 v6, s33, v0
	v_lshlrev_b32_e32 v7, 4, v1
	v_lshlrev_b32_e32 v1, 2, v1
	v_lshlrev_b32_e32 v2, 4, v6
	global_load_dword v39, v1, s[56:57]
	v_lshlrev_b32_e32 v1, 2, v6
	global_load_dwordx4 v[2:5], v2, s[54:55]
	s_nop 0
	global_load_dword v46, v1, s[56:57]
	global_load_dwordx4 v[10:13], v7, s[54:55]
	v_or_b32_e32 v19, 0x800, v0
	v_add_u32_e32 v1, s33, v19
	v_lshlrev_b32_e32 v6, 4, v1
	global_load_dwordx4 v[6:9], v6, s[54:55]
	v_or_b32_e32 v28, 0x1800, v0
	v_add_u32_e32 v20, s33, v28
	v_lshlrev_b32_e32 v1, 2, v1
	v_lshlrev_b32_e32 v14, 2, v20
	global_load_dword v47, v1, s[56:57]
	global_load_dword v27, v14, s[56:57]
	v_or_b32_e32 v48, 0xc00, v0
	v_mul_u32_u24_e32 v14, 0x247, v0
	v_add_u32_e32 v21, s33, v48
	v_lshrrev_b32_e32 v24, 18, v14
	v_lshlrev_b32_e32 v14, 4, v21
	global_load_dwordx4 v[14:17], v14, s[54:55]
	v_lshlrev_b32_e32 v21, 2, v21
	global_load_dword v50, v21, s[56:57]
	v_or_b32_e32 v49, 0x1000, v0
	v_or_b32_e32 v29, 0x1400, v0
	s_movk_i32 s1, 0xfe3e
	v_add_u32_e32 v22, s33, v49
	v_add_u32_e32 v23, s33, v29
	v_mul_u32_u24_e32 v25, 0x91b, v18
	v_mul_u32_u24_e32 v30, 0x1235, v19
	v_lshlrev_b32_e32 v31, 4, v22
	v_lshlrev_b32_e32 v22, 2, v22
	v_lshlrev_b32_e32 v21, 2, v23
	v_lshlrev_b32_e32 v51, 4, v20
	v_mad_i32_i24 v20, v24, s1, v0
	v_lshrrev_b32_e32 v33, 20, v25
	v_lshrrev_b32_e32 v52, 21, v30
	v_lshlrev_b32_e32 v32, 4, v23
	global_load_dword v53, v22, s[56:57]
	global_load_dword v54, v21, s[56:57]
	v_lshl_or_b32 v30, v20, 4, v24
	v_mad_i32_i24 v34, v33, s1, v18
	v_mad_i32_i24 v55, v52, s1, v19
	global_load_dwordx4 v[18:21], v31, s[54:55]
	global_load_dwordx4 v[22:25], v32, s[54:55]
	v_mov_b32_e32 v1, 0x1c200
	v_lshlrev_b32_e32 v56, 4, v30
	v_lshl_add_u32 v57, v30, 2, v1
	v_lshl_or_b32 v30, v34, 4, v33
	v_lshlrev_b32_e32 v58, 4, v30
	v_lshl_add_u32 v59, v30, 2, v1
	s_movk_i32 s0, 0x1c20
	v_or_b32_e32 v26, 0x1c00, v0
	v_cmp_gt_u32_e32 vcc, s0, v26
	v_min_u32_e32 v113, 0x1c1f, v26
	v_add_u32_e32 v113, s33, v113
	v_lshlrev_b32_e32 v114, 4, v113
	v_lshlrev_b32_e32 v113, 2, v113
	global_load_dword v112, v113, s[56:57]
	global_load_dwordx4 v[108:111], v114, s[54:55]
	s_waitcnt vmcnt(12)
	v_cvt_f16_f32_e32 v61, v39
	s_waitcnt vmcnt(10)
	v_cvt_f16_f32_e32 v60, v46
	v_cvt_pk_f16_f32 v30, v2, v3
	v_cvt_f32_f16_e32 v32, v30
	v_cvt_f32_f16_sdwa v33, v30 dst_sel:DWORD dst_unused:UNUSED_PAD src0_sel:WORD_1
	s_waitcnt vmcnt(9)
	v_cvt_pk_f16_f32 v34, v10, v11
	v_cvt_pk_f16_f32 v31, v4, v5
	v_cvt_f32_f16_e32 v40, v34
	v_cvt_f32_f16_sdwa v41, v34 dst_sel:DWORD dst_unused:UNUSED_PAD src0_sel:WORD_1
	v_cvt_f32_f16_e32 v36, v31
	v_cvt_f32_f16_sdwa v37, v31 dst_sel:DWORD dst_unused:UNUSED_PAD src0_sel:WORD_1
	v_cvt_pk_f16_f32 v35, v12, v13
	v_cvt_f32_f16_e32 v60, v60
	v_cvt_f32_f16_e32 v61, v61
	s_waitcnt vmcnt(8)
	v_cvt_pk_f16_f32 v38, v6, v7
	v_cvt_f32_f16_e32 v42, v35
	v_cvt_f32_f16_sdwa v43, v35 dst_sel:DWORD dst_unused:UNUSED_PAD src0_sel:WORD_1
	v_cvt_f32_f16_e32 v44, v38
	v_cvt_f32_f16_sdwa v45, v38 dst_sel:DWORD dst_unused:UNUSED_PAD src0_sel:WORD_1
	v_pk_add_f32 v[2:3], v[2:3], v[32:33] neg_lo:[0,1] neg_hi:[0,1]
	v_pk_add_f32 v[4:5], v[4:5], v[36:37] neg_lo:[0,1] neg_hi:[0,1]
	v_cvt_pk_f16_f32 v32, v2, v3
	v_pk_add_f32 v[2:3], v[10:11], v[40:41] neg_lo:[0,1] neg_hi:[0,1]
	v_cvt_pk_f16_f32 v33, v4, v5
	v_cvt_pk_f16_f32 v36, v2, v3
	v_sub_f32_e32 v2, v46, v60
	v_sub_f32_e32 v3, v39, v61
	v_pk_add_f32 v[4:5], v[12:13], v[42:43] neg_lo:[0,1] neg_hi:[0,1]
	v_cvt_pk_f16_f32 v2, v46, v2
	v_cvt_pk_f16_f32 v3, v39, v3
	ds_write_b128 v56, v[30:33]
	v_cvt_pk_f16_f32 v37, v4, v5
	ds_write_b32 v57, v2
	ds_write_b128 v58, v[34:37]
	ds_write_b32 v59, v3
	v_pk_add_f32 v[2:3], v[6:7], v[44:45] neg_lo:[0,1] neg_hi:[0,1]
	v_cvt_pk_f16_f32 v39, v8, v9
	v_cvt_pk_f16_f32 v40, v2, v3
	global_load_dwordx4 v[2:5], v51, s[54:55]
	v_cvt_f32_f16_e32 v6, v39
	v_cvt_f32_f16_sdwa v7, v39 dst_sel:DWORD dst_unused:UNUSED_PAD src0_sel:WORD_1
	s_waitcnt vmcnt(8)
	v_cvt_f16_f32_e32 v10, v47
	v_pk_add_f32 v[6:7], v[8:9], v[6:7] neg_lo:[0,1] neg_hi:[0,1]
	s_nop 0
	v_cvt_pk_f16_f32 v41, v6, v7
	v_cvt_f32_f16_e32 v6, v10
	v_lshl_or_b32 v7, v55, 4, v52
	v_lshlrev_b32_e32 v8, 4, v7
	v_lshl_add_u32 v7, v7, 2, v1
	v_sub_f32_e32 v6, v47, v6
	v_cvt_pk_f16_f32 v6, v47, v6
	ds_write_b128 v8, v[38:41]
	ds_write_b32 v7, v6
	v_mul_u32_u24_e32 v6, 0x1235, v48
	v_lshrrev_b32_e32 v12, 21, v6
	s_waitcnt vmcnt(6)
	v_cvt_pk_f16_f32 v6, v14, v15
	v_cvt_f32_f16_e32 v8, v6
	v_cvt_f32_f16_sdwa v9, v6 dst_sel:DWORD dst_unused:UNUSED_PAD src0_sel:WORD_1
	v_cvt_pk_f16_f32 v7, v16, v17
	v_cvt_f32_f16_e32 v10, v7
	v_cvt_f32_f16_sdwa v11, v7 dst_sel:DWORD dst_unused:UNUSED_PAD src0_sel:WORD_1
	v_pk_add_f32 v[8:9], v[14:15], v[8:9] neg_lo:[0,1] neg_hi:[0,1]
	s_waitcnt vmcnt(5)
	v_cvt_f16_f32_e32 v14, v50
	v_cvt_pk_f16_f32 v8, v8, v9
	v_pk_add_f32 v[10:11], v[16:17], v[10:11] neg_lo:[0,1] neg_hi:[0,1]
	v_mad_i32_i24 v13, v12, s1, v48
	v_cvt_pk_f16_f32 v9, v10, v11
	v_cvt_f32_f16_e32 v10, v14
	v_lshl_or_b32 v11, v13, 4, v12
	v_lshlrev_b32_e32 v12, 4, v11
	ds_write_b128 v12, v[6:9]
	v_sub_f32_e32 v6, v50, v10
	v_cvt_pk_f16_f32 v6, v50, v6
	v_lshl_add_u32 v7, v11, 2, v1
	ds_write_b32 v7, v6
	v_mul_u32_u24_e32 v6, 0x2469, v49
	v_lshrrev_b32_e32 v12, 22, v6
	s_waitcnt vmcnt(2)
	v_cvt_pk_f16_f32 v6, v18, v19
	v_cvt_pk_f16_f32 v7, v20, v21
	v_cvt_f32_f16_e32 v8, v6
	v_cvt_f32_f16_sdwa v9, v6 dst_sel:DWORD dst_unused:UNUSED_PAD src0_sel:WORD_1
	v_cvt_f32_f16_e32 v10, v7
	v_cvt_f32_f16_sdwa v11, v7 dst_sel:DWORD dst_unused:UNUSED_PAD src0_sel:WORD_1
	v_cvt_f16_f32_e32 v14, v53
	v_pk_add_f32 v[8:9], v[18:19], v[8:9] neg_lo:[0,1] neg_hi:[0,1]
	v_mad_i32_i24 v13, v12, s1, v49
	v_pk_add_f32 v[10:11], v[20:21], v[10:11] neg_lo:[0,1] neg_hi:[0,1]
	v_cvt_pk_f16_f32 v8, v8, v9
	v_cvt_pk_f16_f32 v9, v10, v11
	v_cvt_f32_f16_e32 v10, v14
	v_lshl_or_b32 v11, v13, 4, v12
	v_lshlrev_b32_e32 v12, 4, v11
	ds_write_b128 v12, v[6:9]
	v_sub_f32_e32 v6, v53, v10
	v_cvt_pk_f16_f32 v6, v53, v6
	v_lshl_add_u32 v7, v11, 2, v1
	ds_write_b32 v7, v6
	v_mul_u32_u24_e32 v6, 0x2469, v29
	v_lshrrev_b32_e32 v12, 22, v6
	s_waitcnt vmcnt(1)
	v_cvt_pk_f16_f32 v6, v22, v23
	v_cvt_pk_f16_f32 v7, v24, v25
	v_cvt_f32_f16_e32 v8, v6
	v_cvt_f32_f16_sdwa v9, v6 dst_sel:DWORD dst_unused:UNUSED_PAD src0_sel:WORD_1
	v_cvt_f32_f16_e32 v10, v7
	v_cvt_f32_f16_sdwa v11, v7 dst_sel:DWORD dst_unused:UNUSED_PAD src0_sel:WORD_1
	v_cvt_f16_f32_e32 v14, v54
	v_pk_add_f32 v[8:9], v[22:23], v[8:9] neg_lo:[0,1] neg_hi:[0,1]
	v_mad_i32_i24 v13, v12, s1, v29
	v_pk_add_f32 v[10:11], v[24:25], v[10:11] neg_lo:[0,1] neg_hi:[0,1]
	v_cvt_pk_f16_f32 v8, v8, v9
	v_cvt_pk_f16_f32 v9, v10, v11
	v_cvt_f32_f16_e32 v10, v14
	v_lshl_or_b32 v11, v13, 4, v12
	v_lshlrev_b32_e32 v12, 4, v11
	ds_write_b128 v12, v[6:9]
	v_sub_f32_e32 v6, v54, v10
	v_cvt_pk_f16_f32 v6, v54, v6
	v_lshl_add_u32 v7, v11, 2, v1
	ds_write_b32 v7, v6
	v_mul_u32_u24_e32 v6, 0x2469, v28
	v_lshrrev_b32_e32 v12, 22, v6
	s_waitcnt vmcnt(0)
	v_cvt_pk_f16_f32 v6, v2, v3
	v_cvt_f32_f16_e32 v8, v6
	v_cvt_f32_f16_sdwa v9, v6 dst_sel:DWORD dst_unused:UNUSED_PAD src0_sel:WORD_1
	v_cvt_pk_f16_f32 v7, v4, v5
	v_cvt_f32_f16_e32 v10, v7
	v_cvt_f32_f16_sdwa v11, v7 dst_sel:DWORD dst_unused:UNUSED_PAD src0_sel:WORD_1
	v_cvt_f16_f32_e32 v14, v27
	v_pk_add_f32 v[2:3], v[2:3], v[8:9] neg_lo:[0,1] neg_hi:[0,1]
	v_mad_i32_i24 v13, v12, s1, v28
	v_cvt_pk_f16_f32 v8, v2, v3
	v_pk_add_f32 v[2:3], v[4:5], v[10:11] neg_lo:[0,1] neg_hi:[0,1]
	s_nop 0
	v_cvt_pk_f16_f32 v9, v2, v3
	v_cvt_f32_f16_e32 v2, v14
	v_lshl_or_b32 v3, v13, 4, v12
	v_lshlrev_b32_e32 v4, 4, v3
	v_lshl_add_u32 v3, v3, 2, v1
	v_sub_f32_e32 v2, v27, v2
	v_cvt_pk_f16_f32 v2, v27, v2
	ds_write_b128 v4, v[6:9]
	ds_write_b32 v3, v2
	s_and_saveexec_b64 s[0:1], vcc
	s_cbranch_execz .Lk_222
	v_mov_b32_e32 v6, 0x1a2f
	v_lshl_add_u32 v13, v0, 4, v6
	v_lshlrev_b32_e32 v15, 4, v13
	v_lshl_add_u32 v1, v13, 2, v1
	s_waitcnt vmcnt(0)
	v_mov_b32_e32 v12, v112
	v_mov_b32_e32 v2, v108
	v_mov_b32_e32 v3, v109
	v_mov_b32_e32 v4, v110
	v_mov_b32_e32 v5, v111
	v_cvt_f16_f32_e32 v14, v12
	s_waitcnt vmcnt(0)
	v_cvt_pk_f16_f32 v6, v2, v3
	v_cvt_pk_f16_f32 v7, v4, v5
	v_cvt_f32_f16_e32 v8, v6
	v_cvt_f32_f16_sdwa v9, v6 dst_sel:DWORD dst_unused:UNUSED_PAD src0_sel:WORD_1
	v_cvt_f32_f16_e32 v10, v7
	v_cvt_f32_f16_sdwa v11, v7 dst_sel:DWORD dst_unused:UNUSED_PAD src0_sel:WORD_1
	v_cvt_f32_f16_e32 v14, v14
	v_pk_add_f32 v[2:3], v[2:3], v[8:9] neg_lo:[0,1] neg_hi:[0,1]
	v_pk_add_f32 v[4:5], v[4:5], v[10:11] neg_lo:[0,1] neg_hi:[0,1]
	v_cvt_pk_f16_f32 v8, v2, v3
	v_sub_f32_e32 v2, v12, v14
	v_cvt_pk_f16_f32 v9, v4, v5
	v_cvt_pk_f16_f32 v2, v12, v2
	ds_write_b128 v15, v[6:9]
	ds_write_b32 v1, v2
.Lk_222:
	s_or_b64 exec, exec, s[0:1]
	s_bfe_u32 s15, s14, 0x30006
	s_cmpk_gt_u32 s14, 0x1ff
	s_cselect_b64 s[4:5], -1, 0
	s_lshl_b32 s17, s15, 3
	s_cmpk_lt_u32 s14, 0x200
	v_and_b32_e32 v47, 3, v0
	v_lshrrev_b32_e32 v2, 1, v0
	s_cselect_b64 s[10:11], -1, 0
	v_lshlrev_b32_e32 v1, 6, v47
	v_and_b32_e32 v2, 6, v2
	s_and_b64 s[0:1], s[10:11], exec
	v_or3_b32 v12, v1, v2, s17
	v_lshrrev_b32_e32 v54, 4, v80
	v_mov_b32_e32 v51, 0
	s_cselect_b32 s9, s61, s37
	s_cselect_b32 s8, s60, s36
	v_lshlrev_b32_e32 v50, 8, v12
	v_lshl_add_u64 v[2:3], s[8:9], 0, v[50:51]
	v_lshlrev_b32_e32 v50, 5, v54
	s_cselect_b32 s16, 2, 0
	v_lshl_add_u64 v[2:3], v[2:3], 0, v[50:51]
	global_load_dwordx4 v[20:23], v[2:3], off offset:16
	global_load_dwordx4 v[32:35], v[2:3], off
	global_load_dwordx4 v[24:27], v[2:3], off offset:144
	global_load_dwordx4 v[28:31], v[2:3], off offset:128
	v_lshlrev_b32_e32 v1, s16, v12
	s_cselect_b32 s7, s59, s67
	s_cselect_b32 s6, s58, s66
	v_lshlrev_b32_e32 v50, 2, v1
	global_load_dword v58, v50, s[6:7]
	v_mov_b32_e32 v1, 0x23280
	v_lshl_add_u32 v1, v0, 2, v1
	ds_write2st64_b32 v1, v51, v51 offset1:16
	v_mov_b32_e32 v1, 0xbfb8aa3b
	v_mov_b32_e32 v2, 0x4038aa3b
	v_cmp_eq_u32_e32 vcc, 2, v47
	v_mov_b32_e32 v57, 0
	s_nop 0
	v_cndmask_b32_e32 v46, v1, v2, vcc
	v_lshl_add_u64 v[2:3], s[6:7], 0, v[50:51]
	s_and_b64 vcc, exec, s[4:5]
	s_cbranch_vccnz .Lk_224
	global_load_dwordx3 v[100:102], v[2:3], off offset:4
.Lk_224:
	v_cndmask_b32_e64 v1, 0, 1, s[10:11]
	v_cmp_ne_u32_e64 s[0:1], 1, v1
	s_andn2_b64 vcc, exec, s[10:11]
	v_lshlrev_b32_e32 v1, 3, v54
	s_cbranch_vccnz .Lk_226
.Lk_226:
	v_mov_b32_e32 v5, 0
	s_and_b64 vcc, exec, s[0:1]
	v_mov_b32_e32 v59, 0
	s_cbranch_vccnz .Lk_228
.Lk_228:
	s_and_b64 s[10:11], s[10:11], exec
	s_cselect_b32 s13, s63, s39
	s_cselect_b32 s12, s62, s38
	s_cselect_b32 s11, s65, s41
	s_cselect_b32 s10, s64, s40
	s_lshl_b32 s17, s17, 2
	v_lshl_or_b32 v4, v54, 3, s17
	global_load_dword v6, v4, s[12:13]
	global_load_dword v8, v4, s[10:11]
	global_load_dword v7, v4, s[12:13] offset:256
	global_load_dword v9, v4, s[10:11] offset:256
	global_load_dword v10, v4, s[12:13] offset:512
	global_load_dword v48, v4, s[10:11] offset:512
	global_load_dword v49, v4, s[10:11] offset:768
	global_load_dword v11, v4, s[12:13] offset:768
	v_or_b32_e32 v50, 1, v12
	v_lshlrev_b32_e32 v2, 8, v50
	v_mov_b32_e32 v3, v5
	v_lshl_add_u64 v[2:3], s[8:9], 0, v[2:3]
	v_lshlrev_b32_e32 v44, 2, v1
	v_mov_b32_e32 v45, v5
	v_lshl_add_u64 v[2:3], v[2:3], 0, v[44:45]
	global_load_dwordx4 v[12:15], v[2:3], off offset:16
	global_load_dwordx4 v[40:43], v[2:3], off
	global_load_dwordx4 v[16:19], v[2:3], off offset:144
	global_load_dwordx4 v[36:39], v[2:3], off offset:128
	v_lshlrev_b32_e32 v2, s16, v50
	v_lshlrev_b32_e32 v2, 2, v2
	global_load_dword v45, v2, s[6:7]
	v_mov_b32_e32 v3, v5
	v_lshl_add_u64 v[52:53], s[6:7], 0, v[2:3]
	s_and_b64 vcc, exec, s[0:1]
	v_mov_b32_e32 v50, 0
	s_cbranch_vccz .Lk_291
	v_mov_b32_e32 v55, 0
	s_and_b64 vcc, exec, s[0:1]
	v_mov_b32_e32 v56, 0
	s_cbranch_vccz .Lk_292

.Lk_231:
	s_waitcnt vmcnt(0)
	v_mul_f32_e32 v57, v46, v100
	v_mul_f32_e32 v51, v46, v101
	v_mul_f32_e32 v59, v46, v102
	v_mul_f32_e32 v50, v46, v104
	v_mul_f32_e32 v56, v46, v105
	v_mul_f32_e32 v55, v46, v106

.Lpb_np_2:
	s_nop 7
	v_exp_f32_e32 v84, v52
	v_exp_f32_e32 v85, v56
	v_exp_f32_e32 v86, v50
	v_exp_f32_e32 v87, v54
	v_exp_f32_e32 v88, v51
	v_exp_f32_e32 v89, v55
	v_pk_add_f32 v[90:91], v[84:85], 1.0 op_sel_hi:[1,0]
	v_pk_fma_f32 v[92:93], v[84:85], s[0:1], v[58:59] op_sel_hi:[1,0,0]
	v_pk_fma_f32 v[90:91], v[86:87], v[90:91], v[90:91]
	v_pk_fma_f32 v[94:95], v[90:91], v[88:89], v[90:91]
	v_rcp_f32_e32 v94, v94
	v_rcp_f32_e32 v95, v95
	v_pk_fma_f32 v[92:93], v[92:93], v[88:89], v[92:93]
	v_pk_fma_f32 v[92:93], v[40:41], v[90:91], v[92:93]
	v_exp_f32_e32 v96, v53
	v_pk_mul_f32 v[40:41], v[92:93], v[94:95]
	v_exp_f32_e32 v98, v40
	v_exp_f32_e32 v99, v41
	v_exp_f32_e32 v97, v57
	v_pk_add_f32 v[100:101], v[98:99], 1.0 op_sel_hi:[1,0]
	v_pk_fma_f32 v[100:101], v[100:101], v[96:97], v[100:101]
	v_rcp_f32_e32 v100, v100
	v_rcp_f32_e32 v101, v101
	v_pk_add_f32 v[102:103], v[98:99], -1.0 op_sel_hi:[1,0]
	v_pk_mul_f32 v[102:103], v[102:103], v[100:101]
	v_cvt_pk_f16_f32 v126, v102, v103
	ds_write_b32 v79, v126 offset:6144
	s_waitcnt lgkmcnt(1)
	v_and_b32_e32 v60, 0xffff, v64
	v_lshrrev_b32_e32 v62, 16, v64
	s_nop 1
	v_mfma_f32_16x16x32_f16 v[50:53], v[2:5], v[60:63], v[6:9]
	v_mfma_f32_16x16x32_f16 v[54:57], v[26:29], v[60:63], v[30:33]
	s_waitcnt lgkmcnt(0)
	v_add_u32_e32 v39, 0x80, v39
	v_add_u32_e32 v38, 0x400, v38
	.p2align	6

.Lk_291:
	global_load_dwordx3 v[104:106], v[52:53], off offset:4
	v_mov_b32_e32 v55, 0
	s_and_b64 vcc, exec, s[0:1]
	v_mov_b32_e32 v56, 0
	s_cbranch_vccnz .Lk_230
.Lk_292:
	v_lshl_add_u64 v[2:3], s[12:13], 0, v[4:5]
	s_and_b64 vcc, exec, s[0:1]
	v_lshl_add_u64 v[4:5], s[10:11], 0, v[4:5]
	s_cbranch_vccz .Lk_231
	s_branch .Lk_232
.Lk_298:
	s_and_b64 vcc, exec, s[0:1]
	s_cbranch_vccz .Lk_313
	s_setprio 2
	ds_read_b128 v[34:37], v81
	v_mov_b32_e32 v40, 0
	v_mov_b32_e32 v41, 0
	s_mov_b32 s0, 0x4038aa3b
	s_mov_b32 s1, 0
	v_mov_b32_e32 v58, 0xc038aa3b
	v_mov_b32_e32 v59, 0xc038aa3b
	v_mov_b32_e32 v39, v81
	s_mov_b32 s9, 2
	s_waitcnt lgkmcnt(0)
	ds_read_b128 v[42:45], v78 offset:2048
	ds_read_b128 v[46:49], v78 offset:3072
	v_mfma_f32_16x16x32_f16 v[50:53], v[2:5], v[34:37], v[6:9]
	v_mfma_f32_16x16x32_f16 v[54:57], v[26:29], v[34:37], v[30:33]
	s_waitcnt lgkmcnt(1)
	v_mfma_f32_16x16x32_f16 v[50:53], v[18:21], v[42:45], v[50:53]
	v_mfma_f32_16x16x32_f16 v[54:57], v[10:13], v[42:45], v[54:57]
	s_waitcnt lgkmcnt(0)
	v_mfma_f32_16x16x32_f16 v[50:53], v[22:25], v[46:49], v[50:53]
	v_mfma_f32_16x16x32_f16 v[54:57], v[14:17], v[46:49], v[54:57]
	ds_read_b128 v[34:37], v39 offset:256
	s_nop 6
	v_exp_f32_e32 v84, v52
	v_exp_f32_e32 v85, v56
	v_exp_f32_e32 v86, v50
	v_exp_f32_e32 v87, v54
	v_exp_f32_e32 v88, v51
	v_exp_f32_e32 v89, v55
	v_pk_add_f32 v[90:91], v[84:85], 1.0 op_sel_hi:[1,0]
	v_pk_fma_f32 v[92:93], v[84:85], s[0:1], v[58:59] op_sel_hi:[1,0,0]
	v_pk_fma_f32 v[90:91], v[86:87], v[90:91], v[90:91]
	v_pk_fma_f32 v[94:95], v[90:91], v[88:89], v[90:91]
	v_rcp_f32_e32 v94, v94
	v_rcp_f32_e32 v95, v95
	v_pk_fma_f32 v[92:93], v[92:93], v[88:89], v[92:93]
	v_pk_fma_f32 v[92:93], v[40:41], v[90:91], v[92:93]
	v_exp_f32_e32 v96, v53
	v_pk_mul_f32 v[40:41], v[92:93], v[94:95]
	v_exp_f32_e32 v98, v40
	v_exp_f32_e32 v99, v41
	v_exp_f32_e32 v97, v57
	v_pk_add_f32 v[100:101], v[98:99], 1.0 op_sel_hi:[1,0]
	v_pk_fma_f32 v[100:101], v[100:101], v[96:97], v[100:101]
	v_rcp_f32_e32 v100, v100
	v_rcp_f32_e32 v101, v101
	v_pk_add_f32 v[102:103], v[98:99], -1.0 op_sel_hi:[1,0]
	v_pk_mul_f32 v[102:103], v[102:103], v[100:101]
	v_cvt_pk_f16_f32 v104, v102, v103
	ds_write_b32 v79, v104 offset:0
	s_waitcnt lgkmcnt(0)
	s_barrier
	ds_read_b128 v[42:45], v78 offset:0
	ds_read_b128 v[46:49], v78 offset:1024
	v_mfma_f32_16x16x32_f16 v[50:53], v[2:5], v[34:37], v[6:9]
	v_mfma_f32_16x16x32_f16 v[54:57], v[26:29], v[34:37], v[30:33]
	s_waitcnt lgkmcnt(1)
	v_mfma_f32_16x16x32_f16 v[50:53], v[18:21], v[42:45], v[50:53]
	v_mfma_f32_16x16x32_f16 v[54:57], v[10:13], v[42:45], v[54:57]
	s_waitcnt lgkmcnt(0)
	v_mfma_f32_16x16x32_f16 v[50:53], v[22:25], v[46:49], v[50:53]
	v_mfma_f32_16x16x32_f16 v[54:57], v[14:17], v[46:49], v[54:57]
	ds_read_b128 v[34:37], v39 offset:512
	s_nop 6
	v_exp_f32_e32 v84, v52
	v_exp_f32_e32 v85, v56
	v_exp_f32_e32 v86, v50
	v_exp_f32_e32 v87, v54
	v_exp_f32_e32 v88, v51
	v_exp_f32_e32 v89, v55
	v_pk_add_f32 v[90:91], v[84:85], 1.0 op_sel_hi:[1,0]
	v_pk_fma_f32 v[92:93], v[84:85], s[0:1], v[58:59] op_sel_hi:[1,0,0]
	v_pk_fma_f32 v[90:91], v[86:87], v[90:91], v[90:91]
	v_pk_fma_f32 v[94:95], v[90:91], v[88:89], v[90:91]
	v_rcp_f32_e32 v94, v94
	v_rcp_f32_e32 v95, v95
	v_pk_fma_f32 v[92:93], v[92:93], v[88:89], v[92:93]
	v_pk_fma_f32 v[92:93], v[40:41], v[90:91], v[92:93]
	v_exp_f32_e32 v96, v53
	v_pk_mul_f32 v[40:41], v[92:93], v[94:95]
	v_exp_f32_e32 v98, v40
	v_exp_f32_e32 v99, v41
	v_exp_f32_e32 v97, v57
	v_pk_add_f32 v[100:101], v[98:99], 1.0 op_sel_hi:[1,0]
	v_pk_fma_f32 v[100:101], v[100:101], v[96:97], v[100:101]
	v_rcp_f32_e32 v100, v100
	v_rcp_f32_e32 v101, v101
	v_pk_add_f32 v[102:103], v[98:99], -1.0 op_sel_hi:[1,0]
	v_pk_mul_f32 v[102:103], v[102:103], v[100:101]
	v_cvt_pk_f16_f32 v104, v102, v103
	ds_write_b32 v79, v104 offset:2048
	s_waitcnt lgkmcnt(0)
	v_add_u32_e32 v39, 0x200, v39
	.p2align	6
